# P5 router-logits loop hand-scheduled: a trip's loads issued up front / as registers free (one counted wait per k-step instead of ~8 full drains per trip); same MFMA order; placement of later code as v
# speedup vs baseline: 1.0058x; 1.0018x over previous
.LBB0_2087:
	v_lshl_add_u64 v[84:85], s[90:91], 0, v[82:83]
	v_lshl_add_u64 v[90:91], s[90:91], 0, v[80:81]
	v_add_co_u32_e32 v86, vcc, s56, v90
	global_load_dwordx4 v[200:203], v[84:85], off offset:-256
	global_load_dwordx4 v[204:207], v[84:85], off offset:-240
	v_addc_co_u32_e32 v87, vcc, 0, v91, vcc
	v_add_co_u32_e32 v96, vcc, s57, v90
	global_load_dwordx4 v[208:211], v[84:85], off offset:-192
	global_load_dwordx4 v[212:215], v[84:85], off offset:-176
	v_addc_co_u32_e32 v97, vcc, 0, v91, vcc
	v_add_co_u32_e32 v88, vcc, s58, v90
	global_load_dwordx4 v[216:219], v[84:85], off offset:-128
	global_load_dwordx4 v[220:223], v[84:85], off offset:-112
	v_addc_co_u32_e32 v89, vcc, 0, v91, vcc
	v_add_co_u32_e32 v98, vcc, s59, v90
	global_load_dwordx4 v[224:227], v[84:85], off offset:-64
	global_load_dwordx4 v[228:231], v[84:85], off offset:-48
	v_addc_co_u32_e32 v99, vcc, 0, v91, vcc
	v_add_co_u32_e32 v92, vcc, s60, v90
	global_load_dwordx4 v[34:37], v[84:85], off
	global_load_dwordx4 v[38:41], v[84:85], off offset:16
	v_addc_co_u32_e32 v93, vcc, 0, v91, vcc
	v_add_co_u32_e32 v246, vcc, s61, v90
	global_load_dwordx4 v[42:45], v[84:85], off offset:64
	global_load_dwordx4 v[46:49], v[84:85], off offset:80
	v_addc_co_u32_e32 v247, vcc, 0, v91, vcc
	v_add_co_u32_e32 v94, vcc, s62, v90
	s_nop 1
	v_addc_co_u32_e32 v95, vcc, 0, v91, vcc
	v_add_co_u32_e32 v248, vcc, s63, v90
	s_nop 1
	v_addc_co_u32_e32 v249, vcc, 0, v91, vcc
	v_lshl_add_u64 v[80:81], v[80:81], 0, s[36:37]
	v_lshl_add_u64 v[82:83], v[82:83], 0, s[38:39]
	global_load_dwordx4 v[120:123], v[86:87], off
	global_load_dwordx4 v[124:127], v[86:87], off offset:512
	global_load_dwordx4 v[128:131], v[96:97], off
	global_load_dwordx4 v[132:135], v[96:97], off offset:512
	global_load_dwordx4 v[136:139], v[86:87], off offset:2048
	global_load_dwordx4 v[140:143], v[86:87], off offset:2560
	global_load_dwordx4 v[144:147], v[96:97], off offset:2048
	global_load_dwordx4 v[148:151], v[96:97], off offset:2560
	global_load_dwordx4 v[152:155], v[88:89], off
	global_load_dwordx4 v[156:159], v[88:89], off offset:512
	global_load_dwordx4 v[160:163], v[98:99], off
	global_load_dwordx4 v[164:167], v[98:99], off offset:512
	global_load_dwordx4 v[168:171], v[88:89], off offset:2048
	global_load_dwordx4 v[172:175], v[88:89], off offset:2560
	global_load_dwordx4 v[176:179], v[98:99], off offset:2048
	global_load_dwordx4 v[180:183], v[98:99], off offset:2560
	s_waitcnt vmcnt(12)
	v_cvt_pk_bf16_f32 v236, v200, v201
	v_cvt_pk_bf16_f32 v237, v202, v203
	v_cvt_pk_bf16_f32 v238, v204, v205
	v_cvt_pk_bf16_f32 v239, v206, v207
	v_lshlrev_b32_e32 v244, 16, v236
	v_and_b32_e32 v245, 0xffff0000, v236
	v_mfma_f32_32x32x16_bf16 v[2:17], v[236:239], v[120:123], v[2:17]
	v_mfma_f32_32x32x16_bf16 v[18:33], v[236:239], v[124:127], v[18:33]
	v_pk_add_f32 v[200:201], v[200:201], v[244:245] neg_lo:[0,1] neg_hi:[0,1]
	v_lshlrev_b32_e32 v184, 16, v237
	v_and_b32_e32 v185, 0xffff0000, v237
	v_pk_add_f32 v[202:203], v[202:203], v[184:185] neg_lo:[0,1] neg_hi:[0,1]
	v_lshlrev_b32_e32 v244, 16, v238
	v_and_b32_e32 v245, 0xffff0000, v238
	v_pk_add_f32 v[204:205], v[204:205], v[244:245] neg_lo:[0,1] neg_hi:[0,1]
	v_lshlrev_b32_e32 v184, 16, v239
	v_and_b32_e32 v185, 0xffff0000, v239
	v_pk_add_f32 v[206:207], v[206:207], v[184:185] neg_lo:[0,1] neg_hi:[0,1]
	v_cvt_pk_bf16_f32 v240, v200, v201
	v_cvt_pk_bf16_f32 v241, v202, v203
	v_cvt_pk_bf16_f32 v242, v204, v205
	v_cvt_pk_bf16_f32 v243, v206, v207
	v_mfma_f32_32x32x16_bf16 v[2:17], v[236:239], v[128:131], v[2:17]
	v_mfma_f32_32x32x16_bf16 v[18:33], v[236:239], v[132:135], v[18:33]
	v_mfma_f32_32x32x16_bf16 v[2:17], v[240:243], v[120:123], v[2:17]
	v_mfma_f32_32x32x16_bf16 v[18:33], v[240:243], v[124:127], v[18:33]
	global_load_dwordx4 v[120:123], v[92:93], off
	global_load_dwordx4 v[124:127], v[92:93], off offset:512
	global_load_dwordx4 v[128:131], v[246:247], off
	global_load_dwordx4 v[132:135], v[246:247], off offset:512
	global_load_dwordx4 v[200:203], v[84:85], off offset:128
	global_load_dwordx4 v[204:207], v[84:85], off offset:144
	s_waitcnt vmcnt(14)
	v_cvt_pk_bf16_f32 v236, v208, v209
	v_cvt_pk_bf16_f32 v237, v210, v211
	v_cvt_pk_bf16_f32 v238, v212, v213
	v_cvt_pk_bf16_f32 v239, v214, v215
	v_lshlrev_b32_e32 v244, 16, v236
	v_and_b32_e32 v245, 0xffff0000, v236
	v_mfma_f32_32x32x16_bf16 v[2:17], v[236:239], v[136:139], v[2:17]
	v_mfma_f32_32x32x16_bf16 v[18:33], v[236:239], v[140:143], v[18:33]
	v_pk_add_f32 v[208:209], v[208:209], v[244:245] neg_lo:[0,1] neg_hi:[0,1]
	v_lshlrev_b32_e32 v184, 16, v237
	v_and_b32_e32 v185, 0xffff0000, v237
	v_pk_add_f32 v[210:211], v[210:211], v[184:185] neg_lo:[0,1] neg_hi:[0,1]
	v_lshlrev_b32_e32 v244, 16, v238
	v_and_b32_e32 v245, 0xffff0000, v238
	v_pk_add_f32 v[212:213], v[212:213], v[244:245] neg_lo:[0,1] neg_hi:[0,1]
	v_lshlrev_b32_e32 v184, 16, v239
	v_and_b32_e32 v185, 0xffff0000, v239
	v_pk_add_f32 v[214:215], v[214:215], v[184:185] neg_lo:[0,1] neg_hi:[0,1]
	v_cvt_pk_bf16_f32 v240, v208, v209
	v_cvt_pk_bf16_f32 v241, v210, v211
	v_cvt_pk_bf16_f32 v242, v212, v213
	v_cvt_pk_bf16_f32 v243, v214, v215
	v_mfma_f32_32x32x16_bf16 v[2:17], v[236:239], v[144:147], v[2:17]
	v_mfma_f32_32x32x16_bf16 v[18:33], v[236:239], v[148:151], v[18:33]
	v_mfma_f32_32x32x16_bf16 v[2:17], v[240:243], v[136:139], v[2:17]
	v_mfma_f32_32x32x16_bf16 v[18:33], v[240:243], v[140:143], v[18:33]
	global_load_dwordx4 v[136:139], v[92:93], off offset:2048
	global_load_dwordx4 v[140:143], v[92:93], off offset:2560
	global_load_dwordx4 v[144:147], v[246:247], off offset:2048
	global_load_dwordx4 v[148:151], v[246:247], off offset:2560
	global_load_dwordx4 v[208:211], v[84:85], off offset:192
	global_load_dwordx4 v[212:215], v[84:85], off offset:208
	s_waitcnt vmcnt(16)
	v_cvt_pk_bf16_f32 v236, v216, v217
	v_cvt_pk_bf16_f32 v237, v218, v219
	v_cvt_pk_bf16_f32 v238, v220, v221
	v_cvt_pk_bf16_f32 v239, v222, v223
	v_lshlrev_b32_e32 v244, 16, v236
	v_and_b32_e32 v245, 0xffff0000, v236
	v_mfma_f32_32x32x16_bf16 v[2:17], v[236:239], v[152:155], v[2:17]
	v_mfma_f32_32x32x16_bf16 v[18:33], v[236:239], v[156:159], v[18:33]
	v_pk_add_f32 v[216:217], v[216:217], v[244:245] neg_lo:[0,1] neg_hi:[0,1]
	v_lshlrev_b32_e32 v184, 16, v237
	v_and_b32_e32 v185, 0xffff0000, v237
	v_pk_add_f32 v[218:219], v[218:219], v[184:185] neg_lo:[0,1] neg_hi:[0,1]
	v_lshlrev_b32_e32 v244, 16, v238
	v_and_b32_e32 v245, 0xffff0000, v238
	v_pk_add_f32 v[220:221], v[220:221], v[244:245] neg_lo:[0,1] neg_hi:[0,1]
	v_lshlrev_b32_e32 v184, 16, v239
	v_and_b32_e32 v185, 0xffff0000, v239
	v_pk_add_f32 v[222:223], v[222:223], v[184:185] neg_lo:[0,1] neg_hi:[0,1]
	v_cvt_pk_bf16_f32 v240, v216, v217
	v_cvt_pk_bf16_f32 v241, v218, v219
	v_cvt_pk_bf16_f32 v242, v220, v221
	v_cvt_pk_bf16_f32 v243, v222, v223
	v_mfma_f32_32x32x16_bf16 v[2:17], v[236:239], v[160:163], v[2:17]
	v_mfma_f32_32x32x16_bf16 v[18:33], v[236:239], v[164:167], v[18:33]
	v_mfma_f32_32x32x16_bf16 v[2:17], v[240:243], v[152:155], v[2:17]
	v_mfma_f32_32x32x16_bf16 v[18:33], v[240:243], v[156:159], v[18:33]
	global_load_dwordx4 v[152:155], v[94:95], off
	global_load_dwordx4 v[156:159], v[94:95], off offset:512
	global_load_dwordx4 v[160:163], v[248:249], off
	global_load_dwordx4 v[164:167], v[248:249], off offset:512
	s_waitcnt vmcnt(16)
	v_cvt_pk_bf16_f32 v236, v224, v225
	v_cvt_pk_bf16_f32 v237, v226, v227
	v_cvt_pk_bf16_f32 v238, v228, v229
	v_cvt_pk_bf16_f32 v239, v230, v231
	v_lshlrev_b32_e32 v244, 16, v236
	v_and_b32_e32 v245, 0xffff0000, v236
	v_mfma_f32_32x32x16_bf16 v[2:17], v[236:239], v[168:171], v[2:17]
	v_mfma_f32_32x32x16_bf16 v[18:33], v[236:239], v[172:175], v[18:33]
	v_pk_add_f32 v[224:225], v[224:225], v[244:245] neg_lo:[0,1] neg_hi:[0,1]
	v_lshlrev_b32_e32 v184, 16, v237
	v_and_b32_e32 v185, 0xffff0000, v237
	v_pk_add_f32 v[226:227], v[226:227], v[184:185] neg_lo:[0,1] neg_hi:[0,1]
	v_lshlrev_b32_e32 v244, 16, v238
	v_and_b32_e32 v245, 0xffff0000, v238
	v_pk_add_f32 v[228:229], v[228:229], v[244:245] neg_lo:[0,1] neg_hi:[0,1]
	v_lshlrev_b32_e32 v184, 16, v239
	v_and_b32_e32 v185, 0xffff0000, v239
	v_pk_add_f32 v[230:231], v[230:231], v[184:185] neg_lo:[0,1] neg_hi:[0,1]
	v_cvt_pk_bf16_f32 v240, v224, v225
	v_cvt_pk_bf16_f32 v241, v226, v227
	v_cvt_pk_bf16_f32 v242, v228, v229
	v_cvt_pk_bf16_f32 v243, v230, v231
	v_mfma_f32_32x32x16_bf16 v[2:17], v[236:239], v[176:179], v[2:17]
	v_mfma_f32_32x32x16_bf16 v[18:33], v[236:239], v[180:183], v[18:33]
	v_mfma_f32_32x32x16_bf16 v[2:17], v[240:243], v[168:171], v[2:17]
	v_mfma_f32_32x32x16_bf16 v[18:33], v[240:243], v[172:175], v[18:33]
	global_load_dwordx4 v[168:171], v[94:95], off offset:2048
	global_load_dwordx4 v[172:175], v[94:95], off offset:2560
	global_load_dwordx4 v[176:179], v[248:249], off offset:2048
	global_load_dwordx4 v[180:183], v[248:249], off offset:2560
	s_waitcnt vmcnt(16)
	v_cvt_pk_bf16_f32 v236, v34, v35
	v_cvt_pk_bf16_f32 v237, v36, v37
	v_cvt_pk_bf16_f32 v238, v38, v39
	v_cvt_pk_bf16_f32 v239, v40, v41
	v_lshlrev_b32_e32 v244, 16, v236
	v_and_b32_e32 v245, 0xffff0000, v236
	v_mfma_f32_32x32x16_bf16 v[2:17], v[236:239], v[120:123], v[2:17]
	v_mfma_f32_32x32x16_bf16 v[18:33], v[236:239], v[124:127], v[18:33]
	v_pk_add_f32 v[34:35], v[34:35], v[244:245] neg_lo:[0,1] neg_hi:[0,1]
	v_lshlrev_b32_e32 v184, 16, v237
	v_and_b32_e32 v185, 0xffff0000, v237
	v_pk_add_f32 v[36:37], v[36:37], v[184:185] neg_lo:[0,1] neg_hi:[0,1]
	v_lshlrev_b32_e32 v244, 16, v238
	v_and_b32_e32 v245, 0xffff0000, v238
	v_pk_add_f32 v[38:39], v[38:39], v[244:245] neg_lo:[0,1] neg_hi:[0,1]
	v_lshlrev_b32_e32 v184, 16, v239
	v_and_b32_e32 v185, 0xffff0000, v239
	v_pk_add_f32 v[40:41], v[40:41], v[184:185] neg_lo:[0,1] neg_hi:[0,1]
	v_cvt_pk_bf16_f32 v240, v34, v35
	v_cvt_pk_bf16_f32 v241, v36, v37
	v_cvt_pk_bf16_f32 v242, v38, v39
	v_cvt_pk_bf16_f32 v243, v40, v41
	v_mfma_f32_32x32x16_bf16 v[2:17], v[236:239], v[128:131], v[2:17]
	v_mfma_f32_32x32x16_bf16 v[18:33], v[236:239], v[132:135], v[18:33]
	v_mfma_f32_32x32x16_bf16 v[2:17], v[240:243], v[120:123], v[2:17]
	v_mfma_f32_32x32x16_bf16 v[18:33], v[240:243], v[124:127], v[18:33]
	s_waitcnt vmcnt(10)
	v_cvt_pk_bf16_f32 v236, v42, v43
	v_cvt_pk_bf16_f32 v237, v44, v45
	v_cvt_pk_bf16_f32 v238, v46, v47
	v_cvt_pk_bf16_f32 v239, v48, v49
	v_lshlrev_b32_e32 v244, 16, v236
	v_and_b32_e32 v245, 0xffff0000, v236
	v_mfma_f32_32x32x16_bf16 v[2:17], v[236:239], v[136:139], v[2:17]
	v_mfma_f32_32x32x16_bf16 v[18:33], v[236:239], v[140:143], v[18:33]
	v_pk_add_f32 v[42:43], v[42:43], v[244:245] neg_lo:[0,1] neg_hi:[0,1]
	v_lshlrev_b32_e32 v184, 16, v237
	v_and_b32_e32 v185, 0xffff0000, v237
	v_pk_add_f32 v[44:45], v[44:45], v[184:185] neg_lo:[0,1] neg_hi:[0,1]
	v_lshlrev_b32_e32 v244, 16, v238
	v_and_b32_e32 v245, 0xffff0000, v238
	v_pk_add_f32 v[46:47], v[46:47], v[244:245] neg_lo:[0,1] neg_hi:[0,1]
	v_lshlrev_b32_e32 v184, 16, v239
	v_and_b32_e32 v185, 0xffff0000, v239
	v_pk_add_f32 v[48:49], v[48:49], v[184:185] neg_lo:[0,1] neg_hi:[0,1]
	v_cvt_pk_bf16_f32 v240, v42, v43
	v_cvt_pk_bf16_f32 v241, v44, v45
	v_cvt_pk_bf16_f32 v242, v46, v47
	v_cvt_pk_bf16_f32 v243, v48, v49
	v_mfma_f32_32x32x16_bf16 v[2:17], v[236:239], v[144:147], v[2:17]
	v_mfma_f32_32x32x16_bf16 v[18:33], v[236:239], v[148:151], v[18:33]
	v_mfma_f32_32x32x16_bf16 v[2:17], v[240:243], v[136:139], v[2:17]
	v_mfma_f32_32x32x16_bf16 v[18:33], v[240:243], v[140:143], v[18:33]
	s_waitcnt vmcnt(4)
	v_cvt_pk_bf16_f32 v236, v200, v201
	v_cvt_pk_bf16_f32 v237, v202, v203
	v_cvt_pk_bf16_f32 v238, v204, v205
	v_cvt_pk_bf16_f32 v239, v206, v207
	v_lshlrev_b32_e32 v244, 16, v236
	v_and_b32_e32 v245, 0xffff0000, v236
	v_mfma_f32_32x32x16_bf16 v[2:17], v[236:239], v[152:155], v[2:17]
	v_mfma_f32_32x32x16_bf16 v[18:33], v[236:239], v[156:159], v[18:33]
	v_pk_add_f32 v[200:201], v[200:201], v[244:245] neg_lo:[0,1] neg_hi:[0,1]
	v_lshlrev_b32_e32 v184, 16, v237
	v_and_b32_e32 v185, 0xffff0000, v237
	v_pk_add_f32 v[202:203], v[202:203], v[184:185] neg_lo:[0,1] neg_hi:[0,1]
	v_lshlrev_b32_e32 v244, 16, v238
	v_and_b32_e32 v245, 0xffff0000, v238
	v_pk_add_f32 v[204:205], v[204:205], v[244:245] neg_lo:[0,1] neg_hi:[0,1]
	v_lshlrev_b32_e32 v184, 16, v239
	v_and_b32_e32 v185, 0xffff0000, v239
	v_pk_add_f32 v[206:207], v[206:207], v[184:185] neg_lo:[0,1] neg_hi:[0,1]
	v_cvt_pk_bf16_f32 v240, v200, v201
	v_cvt_pk_bf16_f32 v241, v202, v203
	v_cvt_pk_bf16_f32 v242, v204, v205
	v_cvt_pk_bf16_f32 v243, v206, v207
	v_mfma_f32_32x32x16_bf16 v[2:17], v[236:239], v[160:163], v[2:17]
	v_mfma_f32_32x32x16_bf16 v[18:33], v[236:239], v[164:167], v[18:33]
	v_mfma_f32_32x32x16_bf16 v[2:17], v[240:243], v[152:155], v[2:17]
	v_mfma_f32_32x32x16_bf16 v[18:33], v[240:243], v[156:159], v[18:33]
	s_waitcnt vmcnt(0)
	v_cvt_pk_bf16_f32 v236, v208, v209
	v_cvt_pk_bf16_f32 v237, v210, v211
	v_cvt_pk_bf16_f32 v238, v212, v213
	v_cvt_pk_bf16_f32 v239, v214, v215
	v_lshlrev_b32_e32 v244, 16, v236
	v_and_b32_e32 v245, 0xffff0000, v236
	v_mfma_f32_32x32x16_bf16 v[2:17], v[236:239], v[168:171], v[2:17]
	v_mfma_f32_32x32x16_bf16 v[18:33], v[236:239], v[172:175], v[18:33]
	v_pk_add_f32 v[208:209], v[208:209], v[244:245] neg_lo:[0,1] neg_hi:[0,1]
	v_lshlrev_b32_e32 v184, 16, v237
	v_and_b32_e32 v185, 0xffff0000, v237
	v_pk_add_f32 v[210:211], v[210:211], v[184:185] neg_lo:[0,1] neg_hi:[0,1]
	v_lshlrev_b32_e32 v244, 16, v238
	v_and_b32_e32 v245, 0xffff0000, v238
	v_pk_add_f32 v[212:213], v[212:213], v[244:245] neg_lo:[0,1] neg_hi:[0,1]
	v_lshlrev_b32_e32 v184, 16, v239
	v_and_b32_e32 v185, 0xffff0000, v239
	v_pk_add_f32 v[214:215], v[214:215], v[184:185] neg_lo:[0,1] neg_hi:[0,1]
	v_cvt_pk_bf16_f32 v240, v208, v209
	v_cvt_pk_bf16_f32 v241, v210, v211
	v_cvt_pk_bf16_f32 v242, v212, v213
	v_cvt_pk_bf16_f32 v243, v214, v215
	v_mfma_f32_32x32x16_bf16 v[2:17], v[236:239], v[176:179], v[2:17]
	v_mfma_f32_32x32x16_bf16 v[18:33], v[236:239], v[180:183], v[18:33]
	v_mfma_f32_32x32x16_bf16 v[2:17], v[240:243], v[168:171], v[2:17]
	v_mfma_f32_32x32x16_bf16 v[18:33], v[240:243], v[172:175], v[18:33]
	s_add_i32 s20, s20, -8
	s_cmp_eq_u32 s20, 0
	s_cbranch_scc0 .LBB0_2087
	s_nop 0
	s_nop 0
	s_nop 0
	v_add_u32_e32 v1, 0x800, v114
	s_nop 9
	ds_write2_b32 v114, v2, v18 offset1:32
	ds_write2_b32 v114, v3, v19 offset0:64 offset1:96
	ds_write2_b32 v114, v4, v20 offset0:128 offset1:160
	ds_write2_b32 v114, v5, v21 offset0:192 offset1:224
	ds_write2_b32 v1, v6, v22 offset1:32
	ds_write2_b32 v1, v7, v23 offset0:64 offset1:96
	ds_write2_b32 v1, v8, v24 offset0:128 offset1:160
	ds_write2_b32 v1, v9, v25 offset0:192 offset1:224
	v_add_u32_e32 v1, 0x1000, v114
	ds_write2_b32 v1, v10, v26 offset1:32
	ds_write2_b32 v1, v11, v27 offset0:64 offset1:96
	ds_write2_b32 v1, v12, v28 offset0:128 offset1:160
	ds_write2_b32 v1, v13, v29 offset0:192 offset1:224
	v_add_u32_e32 v1, 0x1800, v114
	ds_write2_b32 v1, v14, v30 offset1:32
	ds_write2_b32 v1, v15, v31 offset0:64 offset1:96
	ds_write2_b32 v1, v16, v32 offset0:128 offset1:160
	ds_write2_b32 v1, v17, v33 offset0:192 offset1:224
	s_waitcnt lgkmcnt(0)
	s_barrier
	ds_read2st64_b32 v[2:3], v104 offset1:8
	ds_read2st64_b32 v[4:5], v104 offset0:32 offset1:40
	ds_read2st64_b32 v[6:7], v104 offset0:64 offset1:72
	ds_read2st64_b32 v[8:9], v104 offset0:96 offset1:104
	ds_read2st64_b32 v[10:11], v104 offset0:128 offset1:136
	ds_read2st64_b32 v[12:13], v104 offset0:160 offset1:168
	ds_read2st64_b32 v[14:15], v104 offset0:192 offset1:200
	s_waitcnt lgkmcnt(6)
	v_add_f32_e32 v1, 0, v2
	s_waitcnt lgkmcnt(5)
	v_add_f32_e32 v1, v1, v4
	s_waitcnt lgkmcnt(4)
	v_add_f32_e32 v1, v1, v6
	ds_read2st64_b32 v[16:17], v104 offset0:224 offset1:232
	s_waitcnt lgkmcnt(4)
	v_add_f32_e32 v1, v1, v8
	ds_read_b32 v2, v105
	s_waitcnt lgkmcnt(4)
	v_add_f32_e32 v1, v1, v10
	s_waitcnt lgkmcnt(3)
	v_add_f32_e32 v1, v1, v12
	s_waitcnt lgkmcnt(2)
	v_add_f32_e32 v1, v1, v14
	s_waitcnt lgkmcnt(1)
	v_add_f32_e32 v1, v1, v16
	s_waitcnt lgkmcnt(0)
	v_mul_f32_e32 v1, v1, v2
	ds_read_b32 v8, v107
	ds_read_b32 v18, v109
	ds_read_b32 v19, v111
	ds_write_b32 v106, v1
	v_add_f32_e32 v1, 0, v3
	v_add_f32_e32 v1, v1, v5
	v_add_f32_e32 v1, v1, v7
	v_add_f32_e32 v1, v1, v9
	v_add_f32_e32 v1, v1, v11
	v_add_f32_e32 v1, v1, v13
	v_add_f32_e32 v1, v1, v15
	ds_read2st64_b32 v[2:3], v104 offset0:16 offset1:24
	ds_read2st64_b32 v[4:5], v104 offset0:48 offset1:56
	ds_read2st64_b32 v[6:7], v104 offset0:80 offset1:88
	v_add_f32_e32 v1, v1, v17
	s_waitcnt lgkmcnt(6)
	v_mul_f32_e32 v1, v1, v8
	ds_write_b32 v108, v1
	s_waitcnt lgkmcnt(3)
	v_add_f32_e32 v1, 0, v2
	s_waitcnt lgkmcnt(2)
	v_add_f32_e32 v1, v1, v4
	s_waitcnt lgkmcnt(1)
	v_add_f32_e32 v1, v1, v6
	ds_read2st64_b32 v[8:9], v104 offset0:112 offset1:120
	ds_read2st64_b32 v[10:11], v104 offset0:144 offset1:152
	ds_read2st64_b32 v[12:13], v104 offset0:176 offset1:184
	ds_read2st64_b32 v[14:15], v104 offset0:208 offset1:216
	ds_read2st64_b32 v[16:17], v104 offset0:240 offset1:248
	s_waitcnt lgkmcnt(4)
	v_add_f32_e32 v1, v1, v8
	s_waitcnt lgkmcnt(3)
	v_add_f32_e32 v1, v1, v10
	s_waitcnt lgkmcnt(2)
	v_add_f32_e32 v1, v1, v12
	s_waitcnt lgkmcnt(1)
	v_add_f32_e32 v1, v1, v14
	s_waitcnt lgkmcnt(0)
	v_add_f32_e32 v1, v1, v16
	v_mul_f32_e32 v1, v1, v18
	ds_write_b32 v110, v1
	v_add_f32_e32 v1, 0, v3
	v_add_f32_e32 v1, v1, v5
	v_add_f32_e32 v1, v1, v7
	v_add_f32_e32 v1, v1, v9
	v_add_f32_e32 v1, v1, v11
	v_add_f32_e32 v1, v1, v13
	v_add_f32_e32 v1, v1, v15
	v_add_f32_e32 v1, v1, v17
	v_mul_f32_e32 v1, v1, v19
	ds_write_b32 v112, v1
	s_waitcnt lgkmcnt(0)
	s_barrier
	global_load_dword v3, v[60:61], off
	ds_read_b32 v1, v119
	s_waitcnt lgkmcnt(0)
	v_mul_f32_e32 v1, 0xbfb8aa3b, v1
	v_exp_f32_e32 v1, v1
	s_nop 0
	v_add_f32_e32 v1, 1.0, v1
	v_div_scale_f32 v2, s[20:21], v1, v1, 1.0
	v_rcp_f32_e32 v4, v2
	s_nop 0
	v_fma_f32 v5, -v2, v4, 1.0
	v_fmac_f32_e32 v4, v5, v4
	v_div_scale_f32 v5, vcc, 1.0, v1, 1.0
	v_mul_f32_e32 v6, v5, v4
	v_fma_f32 v7, -v2, v6, v5
	v_fmac_f32_e32 v6, v7, v4
	v_fma_f32 v2, -v2, v6, v5
	v_div_fmas_f32 v2, v2, v4, v6
	v_div_fixup_f32 v5, v2, v1, 1.0
	s_waitcnt vmcnt(0)
	v_add_f32_e32 v1, v3, v5
	s_nop 1
	v_mov_b32_dpp v2, v1 quad_perm:[1,0,3,2] row_mask:0xf bank_mask:0xf bound_ctrl:1
	v_max_f32_e32 v2, v2, v2
	v_max_f32_e32 v2, v1, v2
	s_nop 1
	v_mov_b32_dpp v4, v2 quad_perm:[2,3,0,1] row_mask:0xf bank_mask:0xf bound_ctrl:1
	v_max_f32_e32 v4, v4, v4
	v_max_f32_e32 v2, v2, v4
	s_nop 1
	v_mov_b32_dpp v4, v2 row_half_mirror row_mask:0xf bank_mask:0xf bound_ctrl:1
	v_max_f32_e32 v4, v4, v4
	v_max_f32_e32 v2, v2, v4
	v_cmp_eq_f32_e32 vcc, v1, v2
	s_nop 1
	v_and_b32_e32 v4, vcc_hi, v63
	v_and_b32_e32 v6, vcc_lo, v62
	v_ffbl_b32_e32 v4, v4
	v_add_u32_e32 v4, 32, v4
	v_ffbl_b32_e32 v6, v6
	v_min_u32_e32 v4, v6, v4
	v_cmp_ne_u32_e32 vcc, v198, v4
	s_nop 1
	v_cndmask_b32_e32 v4, v115, v1, vcc
	s_nop 1
	v_mov_b32_dpp v6, v4 quad_perm:[1,0,3,2] row_mask:0xf bank_mask:0xf bound_ctrl:1
	v_max_f32_e32 v6, v6, v6
	v_max_f32_e32 v4, v4, v6
	s_nop 1
	v_mov_b32_dpp v6, v4 quad_perm:[2,3,0,1] row_mask:0xf bank_mask:0xf bound_ctrl:1
	v_max_f32_e32 v6, v6, v6
	v_max_f32_e32 v4, v4, v6
	s_nop 1
	v_mov_b32_dpp v6, v4 row_half_mirror row_mask:0xf bank_mask:0xf bound_ctrl:1
	v_max_f32_e32 v6, v6, v6
	v_max_f32_e32 v4, v4, v6
	v_add_f32_e32 v2, v2, v4
	s_nop 0
	v_readlane_b32 s20, v2, 0
	s_nop 1
	v_cmp_gt_f32_e32 vcc, s20, v2
	v_cmp_eq_f32_e64 s[20:21], s20, v2
	s_and_b64 s[20:21], s[20:21], s[6:7]
	s_or_b64 s[20:21], vcc, s[20:21]
	v_cndmask_b32_e64 v4, 0, 1, s[20:21]
	v_readlane_b32 s20, v2, 8
	s_nop 1
	v_cmp_gt_f32_e32 vcc, s20, v2
	v_cmp_eq_f32_e64 s[20:21], s20, v2
	s_and_b64 s[20:21], s[20:21], s[8:9]
	s_or_b64 s[20:21], vcc, s[20:21]
	v_cndmask_b32_e64 v6, 0, 1, s[20:21]
	v_readlane_b32 s20, v2, 16
	s_nop 1
	v_cmp_gt_f32_e32 vcc, s20, v2
	v_cmp_eq_f32_e64 s[20:21], s20, v2
	s_and_b64 s[20:21], s[20:21], s[10:11]
	s_or_b64 s[20:21], vcc, s[20:21]
	v_cndmask_b32_e64 v7, 0, 1, s[20:21]
	v_readlane_b32 s20, v2, 24
	v_add3_u32 v4, v4, v6, v7
	s_nop 0
	v_cmp_gt_f32_e32 vcc, s20, v2
	v_cmp_eq_f32_e64 s[20:21], s20, v2
	s_and_b64 s[20:21], s[20:21], s[12:13]
	s_or_b64 s[20:21], vcc, s[20:21]
	v_cndmask_b32_e64 v6, 0, 1, s[20:21]
	v_readlane_b32 s20, v2, 32
	s_nop 1
	v_cmp_gt_f32_e32 vcc, s20, v2
	v_cmp_eq_f32_e64 s[20:21], s20, v2
	s_and_b64 s[20:21], s[20:21], s[14:15]
	s_or_b64 s[20:21], vcc, s[20:21]
	v_cndmask_b32_e64 v7, 0, 1, s[20:21]
	v_readlane_b32 s20, v2, 40
	v_add3_u32 v4, v4, v6, v7
	s_nop 0
	v_cmp_gt_f32_e32 vcc, s20, v2
	v_cmp_eq_f32_e64 s[20:21], s20, v2
	s_and_b64 s[20:21], s[20:21], s[16:17]
	s_or_b64 s[20:21], vcc, s[20:21]
	v_cndmask_b32_e64 v6, 0, 1, s[20:21]
	v_readlane_b32 s20, v2, 48
	s_nop 1
	v_cmp_gt_f32_e32 vcc, s20, v2
	v_cmp_eq_f32_e64 s[20:21], s20, v2
	s_and_b64 s[20:21], s[18:19], s[20:21]
	s_or_b64 s[20:21], vcc, s[20:21]
	v_cndmask_b32_e64 v7, 0, 1, s[20:21]
	v_readlane_b32 s20, v2, 56
	s_nop 1
	v_cmp_gt_f32_e32 vcc, s20, v2
	s_nop 1
	v_addc_co_u32_e32 v2, vcc, v4, v6, vcc
	v_add_u32_e32 v2, v2, v7
	v_cmp_gt_u32_e32 vcc, 4, v2
	v_mov_b32_e32 v2, 0xff800000
	v_mov_b32_e32 v4, 0xff800000
	v_cndmask_b32_e32 v1, v115, v1, vcc
	v_mov_b32_e32 v6, 0xff800000
	s_nop 0
	v_mov_b32_dpp v2, v1 row_shr:1 row_mask:0xf bank_mask:0xf
	v_max_f32_e32 v2, v2, v2
	v_max_f32_e32 v2, v1, v2
	s_nop 1
	v_mov_b32_dpp v4, v2 row_shr:2 row_mask:0xf bank_mask:0xf
	v_max_f32_e32 v4, v4, v4
	v_max_f32_e32 v2, v2, v4
	v_mov_b32_e32 v4, 0xff800000
	s_nop 1
	v_mov_b32_dpp v4, v2 row_shr:4 row_mask:0xf bank_mask:0xf
	v_max_f32_e32 v4, v4, v4
	v_max_f32_e32 v2, v2, v4
	v_mov_b32_e32 v4, 0xff800000
	s_nop 1
	v_mov_b32_dpp v4, v2 row_shr:8 row_mask:0xf bank_mask:0xf
	v_max_f32_e32 v4, v4, v4
	v_max_f32_e32 v2, v2, v4
	v_mov_b32_e32 v4, 0xff800000
	s_nop 1
	v_mov_b32_dpp v4, v2 row_bcast:15 row_mask:0xa bank_mask:0xf
	v_max_f32_e32 v4, v4, v4
	v_max_f32_e32 v2, v2, v4
	v_mov_b32_e32 v4, 0xff800000
	s_nop 1
	v_mov_b32_dpp v4, v2 row_bcast:31 row_mask:0xc bank_mask:0xf
	v_max_f32_e32 v4, v4, v4
	v_max_f32_e32 v2, v2, v4
	v_mov_b32_e32 v4, 0xff800000
	v_readlane_b32 s20, v2, 63
	s_nop 1
	v_cmp_eq_f32_e32 vcc, s20, v1
	s_ff1_i32_b64 s20, vcc
	v_cmp_ne_u32_e32 vcc, s20, v198
	s_nop 1
	v_cndmask_b32_e32 v1, v115, v1, vcc
	v_cndmask_b32_e64 v2, 0, -1, vcc
	s_nop 0
	v_mov_b32_dpp v4, v1 row_shr:1 row_mask:0xf bank_mask:0xf
	v_max_f32_e32 v4, v4, v4
	v_max_f32_e32 v4, v1, v4
	s_nop 1
	v_mov_b32_dpp v6, v4 row_shr:2 row_mask:0xf bank_mask:0xf
	v_max_f32_e32 v6, v6, v6
	v_max_f32_e32 v4, v4, v6
	v_mov_b32_e32 v6, 0xff800000
	s_nop 1
	v_mov_b32_dpp v6, v4 row_shr:4 row_mask:0xf bank_mask:0xf
	v_max_f32_e32 v6, v6, v6
	v_max_f32_e32 v4, v4, v6
	v_mov_b32_e32 v6, 0xff800000
	s_nop 1
	v_mov_b32_dpp v6, v4 row_shr:8 row_mask:0xf bank_mask:0xf
	v_max_f32_e32 v6, v6, v6
	v_max_f32_e32 v4, v4, v6
	v_mov_b32_e32 v6, 0xff800000
	s_nop 1
	v_mov_b32_dpp v6, v4 row_bcast:15 row_mask:0xa bank_mask:0xf
	v_max_f32_e32 v6, v6, v6
	v_max_f32_e32 v4, v4, v6
	v_mov_b32_e32 v6, 0xff800000
	s_nop 1
	v_mov_b32_dpp v6, v4 row_bcast:31 row_mask:0xc bank_mask:0xf
	v_max_f32_e32 v6, v6, v6
	v_max_f32_e32 v4, v4, v6
	v_mov_b32_e32 v6, 0xff800000
	v_readlane_b32 s20, v4, 63
	v_mov_b32_e32 v4, 0xff800000
	s_nop 0
	v_cmp_eq_f32_e32 vcc, s20, v1
	s_ff1_i32_b64 s20, vcc
	v_cmp_eq_u32_e32 vcc, s20, v198
	s_nop 1
	v_cndmask_b32_e32 v1, v1, v115, vcc
	v_cndmask_b32_e64 v2, v2, 1, vcc
	s_nop 0
	v_mov_b32_dpp v4, v1 row_shr:1 row_mask:0xf bank_mask:0xf
	v_max_f32_e32 v4, v4, v4
	v_max_f32_e32 v4, v1, v4
	s_nop 1
	v_mov_b32_dpp v6, v4 row_shr:2 row_mask:0xf bank_mask:0xf
	v_max_f32_e32 v6, v6, v6
	v_max_f32_e32 v4, v4, v6
	v_mov_b32_e32 v6, 0xff800000
	s_nop 1
	v_mov_b32_dpp v6, v4 row_shr:4 row_mask:0xf bank_mask:0xf
	v_max_f32_e32 v6, v6, v6
	v_max_f32_e32 v4, v4, v6
	v_mov_b32_e32 v6, 0xff800000
	s_nop 1
	v_mov_b32_dpp v6, v4 row_shr:8 row_mask:0xf bank_mask:0xf
	v_max_f32_e32 v6, v6, v6
	v_max_f32_e32 v4, v4, v6
	v_mov_b32_e32 v6, 0xff800000
	s_nop 1
	v_mov_b32_dpp v6, v4 row_bcast:15 row_mask:0xa bank_mask:0xf
	v_max_f32_e32 v6, v6, v6
	v_max_f32_e32 v4, v4, v6
	v_mov_b32_e32 v6, 0xff800000
	s_nop 1
	v_mov_b32_dpp v6, v4 row_bcast:31 row_mask:0xc bank_mask:0xf
	v_max_f32_e32 v6, v6, v6
	v_max_f32_e32 v4, v4, v6
	v_mov_b32_e32 v6, 0xff800000
	v_readlane_b32 s20, v4, 63
	v_mov_b32_e32 v4, 0xff800000
	s_nop 0
	v_cmp_eq_f32_e32 vcc, s20, v1
	s_ff1_i32_b64 s20, vcc
	v_cmp_eq_u32_e32 vcc, s20, v198
	s_nop 1
	v_cndmask_b32_e32 v1, v1, v115, vcc
	v_cndmask_b32_e64 v2, v2, 2, vcc
	s_nop 0
	v_mov_b32_dpp v4, v1 row_shr:1 row_mask:0xf bank_mask:0xf
	v_max_f32_e32 v4, v4, v4
	v_max_f32_e32 v4, v1, v4
	s_nop 1
	v_mov_b32_dpp v6, v4 row_shr:2 row_mask:0xf bank_mask:0xf
	v_max_f32_e32 v6, v6, v6
	v_max_f32_e32 v4, v4, v6
	v_mov_b32_e32 v6, 0xff800000
	s_nop 1
	v_mov_b32_dpp v6, v4 row_shr:4 row_mask:0xf bank_mask:0xf
	v_max_f32_e32 v6, v6, v6
	v_max_f32_e32 v4, v4, v6
	v_mov_b32_e32 v6, 0xff800000
	s_nop 1
	v_mov_b32_dpp v6, v4 row_shr:8 row_mask:0xf bank_mask:0xf
	v_max_f32_e32 v6, v6, v6
	v_max_f32_e32 v4, v4, v6
	v_mov_b32_e32 v6, 0xff800000
	s_nop 1
	v_mov_b32_dpp v6, v4 row_bcast:15 row_mask:0xa bank_mask:0xf
	v_max_f32_e32 v6, v6, v6
	v_max_f32_e32 v4, v4, v6
	v_mov_b32_e32 v6, 0xff800000
	s_nop 1
	v_mov_b32_dpp v6, v4 row_bcast:31 row_mask:0xc bank_mask:0xf
	v_max_f32_e32 v6, v6, v6
	v_max_f32_e32 v4, v4, v6
	v_mov_b32_e32 v6, 0xff800000
	v_readlane_b32 s20, v4, 63
	v_mov_b32_e32 v4, 0xff800000
	s_nop 0
	v_cmp_eq_f32_e32 vcc, s20, v1
	s_ff1_i32_b64 s20, vcc
	v_cmp_eq_u32_e32 vcc, s20, v198
	s_nop 1
	v_cndmask_b32_e32 v1, v1, v115, vcc
	v_cndmask_b32_e64 v2, v2, 3, vcc
	s_nop 0
	v_mov_b32_dpp v4, v1 row_shr:1 row_mask:0xf bank_mask:0xf
	v_max_f32_e32 v4, v4, v4
	v_max_f32_e32 v4, v1, v4
	s_nop 1
	v_mov_b32_dpp v6, v4 row_shr:2 row_mask:0xf bank_mask:0xf
	v_max_f32_e32 v6, v6, v6
	v_max_f32_e32 v4, v4, v6
	v_mov_b32_e32 v6, 0xff800000
	s_nop 1
	v_mov_b32_dpp v6, v4 row_shr:4 row_mask:0xf bank_mask:0xf
	v_max_f32_e32 v6, v6, v6
	v_max_f32_e32 v4, v4, v6
	v_mov_b32_e32 v6, 0xff800000
	s_nop 1
	v_mov_b32_dpp v6, v4 row_shr:8 row_mask:0xf bank_mask:0xf
	v_max_f32_e32 v6, v6, v6
	v_max_f32_e32 v4, v4, v6
	v_mov_b32_e32 v6, 0xff800000
	s_nop 1
	v_mov_b32_dpp v6, v4 row_bcast:15 row_mask:0xa bank_mask:0xf
	v_max_f32_e32 v6, v6, v6
	v_max_f32_e32 v4, v4, v6
	v_mov_b32_e32 v6, 0xff800000
	s_nop 1
	v_mov_b32_dpp v6, v4 row_bcast:31 row_mask:0xc bank_mask:0xf
	v_max_f32_e32 v6, v6, v6
	v_max_f32_e32 v4, v4, v6
	s_nop 0
	v_readlane_b32 s20, v4, 63
	v_mov_b32_e32 v4, 0xff800000
	s_nop 0
	v_cmp_eq_f32_e32 vcc, s20, v1
	s_ff1_i32_b64 s20, vcc
	v_cmp_eq_u32_e32 vcc, s20, v198
	s_nop 1
	v_cndmask_b32_e32 v1, v1, v115, vcc
	v_max_f32_e32 v6, v1, v1
	v_cndmask_b32_e64 v2, v2, 4, vcc
	v_mov_b32_dpp v4, v1 row_shr:1 row_mask:0xf bank_mask:0xf
	v_max_f32_e32 v4, v4, v4
	v_max_f32_e32 v4, v6, v4
	v_mov_b32_e32 v6, 0xff800000
	s_nop 1
	v_mov_b32_dpp v6, v4 row_shr:2 row_mask:0xf bank_mask:0xf
	v_max_f32_e32 v6, v6, v6
	v_max_f32_e32 v4, v4, v6
	v_mov_b32_e32 v6, 0xff800000
	s_nop 1
	v_mov_b32_dpp v6, v4 row_shr:4 row_mask:0xf bank_mask:0xf
	v_max_f32_e32 v6, v6, v6
	v_max_f32_e32 v4, v4, v6
	v_mov_b32_e32 v6, 0xff800000
	s_nop 1
	v_mov_b32_dpp v6, v4 row_shr:8 row_mask:0xf bank_mask:0xf
	v_max_f32_e32 v6, v6, v6
	v_max_f32_e32 v4, v4, v6
	v_mov_b32_e32 v6, 0xff800000
	s_nop 1
	v_mov_b32_dpp v6, v4 row_bcast:15 row_mask:0xa bank_mask:0xf
	v_max_f32_e32 v6, v6, v6
	v_max_f32_e32 v4, v4, v6
	v_mov_b32_e32 v6, 0xff800000
	s_nop 1
	v_mov_b32_dpp v6, v4 row_bcast:31 row_mask:0xc bank_mask:0xf
	v_max_f32_e32 v6, v6, v6
	v_max_f32_e32 v4, v4, v6
	s_nop 0
	v_readlane_b32 s20, v4, 63
	v_mov_b32_e32 v4, 0xff800000
	s_nop 0
	v_cmp_eq_f32_e32 vcc, s20, v1
	s_ff1_i32_b64 s20, vcc
	v_cmp_eq_u32_e32 vcc, s20, v198
	s_nop 1
	v_cndmask_b32_e32 v1, v1, v115, vcc
	v_max_f32_e32 v6, v1, v1
	v_cndmask_b32_e64 v2, v2, 5, vcc
	v_mov_b32_dpp v4, v1 row_shr:1 row_mask:0xf bank_mask:0xf
	v_max_f32_e32 v4, v4, v4
	v_max_f32_e32 v4, v6, v4
	v_mov_b32_e32 v6, 0xff800000
	s_nop 1
	v_mov_b32_dpp v6, v4 row_shr:2 row_mask:0xf bank_mask:0xf
	v_max_f32_e32 v6, v6, v6
	v_max_f32_e32 v4, v4, v6
	v_mov_b32_e32 v6, 0xff800000
	s_nop 1
	v_mov_b32_dpp v6, v4 row_shr:4 row_mask:0xf bank_mask:0xf
	v_max_f32_e32 v6, v6, v6
	v_max_f32_e32 v4, v4, v6
	v_mov_b32_e32 v6, 0xff800000
	s_nop 1
	v_mov_b32_dpp v6, v4 row_shr:8 row_mask:0xf bank_mask:0xf
	v_max_f32_e32 v6, v6, v6
	v_max_f32_e32 v4, v4, v6
	v_mov_b32_e32 v6, 0xff800000
	s_nop 1
	v_mov_b32_dpp v6, v4 row_bcast:15 row_mask:0xa bank_mask:0xf
	v_max_f32_e32 v6, v6, v6
	v_max_f32_e32 v4, v4, v6
	v_mov_b32_e32 v6, 0xff800000
	s_nop 1
	v_mov_b32_dpp v6, v4 row_bcast:31 row_mask:0xc bank_mask:0xf
	v_max_f32_e32 v6, v6, v6
	v_max_f32_e32 v4, v4, v6
	s_nop 0
	v_readlane_b32 s20, v4, 63
	v_mov_b32_e32 v4, 0xff800000
	s_nop 0
	v_cmp_eq_f32_e32 vcc, s20, v1
	s_ff1_i32_b64 s20, vcc
	v_cmp_eq_u32_e32 vcc, s20, v198
	s_nop 1
	v_cndmask_b32_e32 v1, v1, v115, vcc
	v_max_f32_e32 v6, v1, v1
	v_cndmask_b32_e64 v2, v2, 6, vcc
	v_mov_b32_dpp v4, v1 row_shr:1 row_mask:0xf bank_mask:0xf
	v_max_f32_e32 v4, v4, v4
	v_max_f32_e32 v4, v6, v4
	v_mov_b32_e32 v6, 0xff800000
	s_nop 1
	v_mov_b32_dpp v6, v4 row_shr:2 row_mask:0xf bank_mask:0xf
	v_max_f32_e32 v6, v6, v6
	v_max_f32_e32 v4, v4, v6
	v_mov_b32_e32 v6, 0xff800000
	s_nop 1
	v_mov_b32_dpp v6, v4 row_shr:4 row_mask:0xf bank_mask:0xf
	v_max_f32_e32 v6, v6, v6
	v_max_f32_e32 v4, v4, v6
	v_mov_b32_e32 v6, 0xff800000
	s_nop 1
	v_mov_b32_dpp v6, v4 row_shr:8 row_mask:0xf bank_mask:0xf
	v_max_f32_e32 v6, v6, v6
	v_max_f32_e32 v4, v4, v6
	v_mov_b32_e32 v6, 0xff800000
	s_nop 1
	v_mov_b32_dpp v6, v4 row_bcast:15 row_mask:0xa bank_mask:0xf
	v_max_f32_e32 v6, v6, v6
	v_max_f32_e32 v4, v4, v6
	v_mov_b32_e32 v6, 0xff800000
	s_nop 1
	v_mov_b32_dpp v6, v4 row_bcast:31 row_mask:0xc bank_mask:0xf
	v_max_f32_e32 v6, v6, v6
	v_max_f32_e32 v4, v4, v6
	s_nop 0
	v_readlane_b32 s20, v4, 63
	s_nop 1
	v_cmp_eq_f32_e32 vcc, s20, v1
	s_ff1_i32_b64 s20, vcc
	v_cmp_ne_u32_e32 vcc, s20, v198
	s_nop 1
	v_cndmask_b32_e32 v6, 7, v2, vcc
	v_cmp_lt_i32_e64 s[20:21], -1, v6
	v_mov_b32_e32 v2, 0
	s_nop 0
	v_cndmask_b32_e64 v1, 0, v5, s[20:21]
	s_nop 1
	v_add_f32_dpp v1, v1, v1 row_shr:1 row_mask:0xf bank_mask:0xf bound_ctrl:1
	s_nop 1
	v_add_f32_dpp v1, v1, v1 row_shr:2 row_mask:0xf bank_mask:0xf bound_ctrl:1
	s_nop 1
	v_add_f32_dpp v1, v1, v1 row_shr:4 row_mask:0xf bank_mask:0xf bound_ctrl:1
	s_nop 1
	v_add_f32_dpp v1, v1, v1 row_shr:8 row_mask:0xf bank_mask:0xf bound_ctrl:1
	s_nop 1
	v_mov_b32_dpp v2, v1 row_bcast:15 row_mask:0xa bank_mask:0xf
	v_add_f32_e32 v1, v1, v2
	v_mov_b32_e32 v2, 0
	s_nop 1
	v_mov_b32_dpp v2, v1 row_bcast:31 row_mask:0xc bank_mask:0xf
	v_add_f32_e32 v1, v1, v2
	v_mov_b32_e32 v2, s35
	v_readlane_b32 s41, v1, 63
	s_and_saveexec_b64 s[22:23], s[20:21]
	ds_add_rtn_u32 v2, v101, v116
	s_or_b64 exec, exec, s[22:23]
	ds_read_b32 v1, v119 offset:256
	s_waitcnt lgkmcnt(0)
	v_mul_f32_e32 v1, 0xbfb8aa3b, v1
	v_exp_f32_e32 v1, v1
	s_nop 0
	v_add_f32_e32 v1, 1.0, v1
	v_div_scale_f32 v4, s[22:23], v1, v1, 1.0
	v_rcp_f32_e32 v7, v4
	v_div_scale_f32 v8, vcc, 1.0, v1, 1.0
	v_fma_f32 v9, -v4, v7, 1.0
	v_fmac_f32_e32 v7, v9, v7
	v_mul_f32_e32 v9, v8, v7
	v_fma_f32 v10, -v4, v9, v8
	v_fmac_f32_e32 v9, v10, v7
	v_fma_f32 v4, -v4, v9, v8
	v_div_fmas_f32 v4, v4, v7, v9
	v_div_fixup_f32 v7, v4, v1, 1.0
	v_add_f32_e32 v1, v3, v7
	s_nop 1
	v_mov_b32_dpp v4, v1 quad_perm:[1,0,3,2] row_mask:0xf bank_mask:0xf bound_ctrl:1
	v_max_f32_e32 v4, v4, v4
	v_max_f32_e32 v4, v1, v4
	s_nop 1
	v_mov_b32_dpp v8, v4 quad_perm:[2,3,0,1] row_mask:0xf bank_mask:0xf bound_ctrl:1
	v_max_f32_e32 v8, v8, v8
	v_max_f32_e32 v4, v4, v8
	s_nop 1
	v_mov_b32_dpp v8, v4 row_half_mirror row_mask:0xf bank_mask:0xf bound_ctrl:1
	v_max_f32_e32 v8, v8, v8
	v_max_f32_e32 v4, v4, v8
	v_cmp_eq_f32_e32 vcc, v1, v4
	s_nop 1
	v_and_b32_e32 v8, vcc_hi, v63
	v_and_b32_e32 v9, vcc_lo, v62
	v_ffbl_b32_e32 v8, v8
	v_ffbl_b32_e32 v9, v9
	v_add_u32_e32 v8, 32, v8
	v_min_u32_e32 v8, v9, v8
	v_cmp_ne_u32_e32 vcc, v198, v8
	s_nop 1
	v_cndmask_b32_e32 v8, v115, v1, vcc
	s_nop 1
	v_mov_b32_dpp v9, v8 quad_perm:[1,0,3,2] row_mask:0xf bank_mask:0xf bound_ctrl:1
	v_max_f32_e32 v9, v9, v9
	v_max_f32_e32 v8, v8, v9
	s_nop 1
	v_mov_b32_dpp v9, v8 quad_perm:[2,3,0,1] row_mask:0xf bank_mask:0xf bound_ctrl:1
	v_max_f32_e32 v9, v9, v9
	v_max_f32_e32 v8, v8, v9
	s_nop 1
	v_mov_b32_dpp v9, v8 row_half_mirror row_mask:0xf bank_mask:0xf bound_ctrl:1
	v_max_f32_e32 v9, v9, v9
	v_max_f32_e32 v8, v8, v9
	v_add_f32_e32 v4, v4, v8
	s_nop 0
	v_readlane_b32 s22, v4, 0
	v_readlane_b32 s24, v4, 8
	s_nop 0
	v_cmp_gt_f32_e32 vcc, s22, v4
	v_cmp_eq_f32_e64 s[22:23], s22, v4
	s_and_b64 s[22:23], s[22:23], s[6:7]
	s_or_b64 s[22:23], vcc, s[22:23]
	v_cndmask_b32_e64 v8, 0, 1, s[22:23]
	v_cmp_eq_f32_e64 s[22:23], s24, v4
	v_cmp_gt_f32_e32 vcc, s24, v4
	s_and_b64 s[22:23], s[22:23], s[8:9]
	s_or_b64 s[22:23], vcc, s[22:23]
	v_cndmask_b32_e64 v9, 0, 1, s[22:23]
	v_readlane_b32 s22, v4, 16
	s_nop 1
	v_cmp_gt_f32_e32 vcc, s22, v4
	v_cmp_eq_f32_e64 s[22:23], s22, v4
	s_and_b64 s[22:23], s[22:23], s[10:11]
	s_or_b64 s[22:23], vcc, s[22:23]
	v_cndmask_b32_e64 v10, 0, 1, s[22:23]
	v_readlane_b32 s22, v4, 24
	v_add3_u32 v8, v8, v9, v10
	s_nop 0
	v_cmp_gt_f32_e32 vcc, s22, v4
	v_cmp_eq_f32_e64 s[22:23], s22, v4
	s_and_b64 s[22:23], s[22:23], s[12:13]
	s_or_b64 s[22:23], vcc, s[22:23]
	v_cndmask_b32_e64 v9, 0, 1, s[22:23]
	v_readlane_b32 s22, v4, 32
	s_nop 1
	v_cmp_gt_f32_e32 vcc, s22, v4
	v_cmp_eq_f32_e64 s[22:23], s22, v4
	s_and_b64 s[22:23], s[22:23], s[14:15]
	s_or_b64 s[22:23], vcc, s[22:23]
	v_cndmask_b32_e64 v10, 0, 1, s[22:23]
	v_readlane_b32 s22, v4, 40
	v_add3_u32 v8, v8, v9, v10
	s_nop 0
	v_cmp_gt_f32_e32 vcc, s22, v4
	v_cmp_eq_f32_e64 s[22:23], s22, v4
	s_and_b64 s[22:23], s[22:23], s[16:17]
	s_or_b64 s[22:23], vcc, s[22:23]
	v_cndmask_b32_e64 v9, 0, 1, s[22:23]
	v_readlane_b32 s22, v4, 48
	s_nop 1
	v_cmp_gt_f32_e32 vcc, s22, v4
	v_cmp_eq_f32_e64 s[22:23], s22, v4
	s_and_b64 s[22:23], s[18:19], s[22:23]
	s_or_b64 s[22:23], vcc, s[22:23]
	v_cndmask_b32_e64 v10, 0, 1, s[22:23]
	v_readlane_b32 s22, v4, 56
	s_nop 1
	v_cmp_gt_f32_e32 vcc, s22, v4
	s_nop 1
	v_addc_co_u32_e32 v4, vcc, v8, v9, vcc
	v_add_u32_e32 v4, v4, v10
	v_cmp_gt_u32_e32 vcc, 4, v4
	v_mov_b32_e32 v4, 0xff800000
	v_mov_b32_e32 v8, 0xff800000
	v_cndmask_b32_e32 v1, v115, v1, vcc
	v_mov_b32_e32 v9, 0xff800000
	s_nop 0
	v_mov_b32_dpp v4, v1 row_shr:1 row_mask:0xf bank_mask:0xf
	v_max_f32_e32 v4, v4, v4
	v_max_f32_e32 v4, v1, v4
	s_nop 1
	v_mov_b32_dpp v8, v4 row_shr:2 row_mask:0xf bank_mask:0xf
	v_max_f32_e32 v8, v8, v8
	v_max_f32_e32 v4, v4, v8
	v_mov_b32_e32 v8, 0xff800000
	s_nop 1
	v_mov_b32_dpp v8, v4 row_shr:4 row_mask:0xf bank_mask:0xf
	v_max_f32_e32 v8, v8, v8
	v_max_f32_e32 v4, v4, v8
	v_mov_b32_e32 v8, 0xff800000
	s_nop 1
	v_mov_b32_dpp v8, v4 row_shr:8 row_mask:0xf bank_mask:0xf
	v_max_f32_e32 v8, v8, v8
	v_max_f32_e32 v4, v4, v8
	v_mov_b32_e32 v8, 0xff800000
	s_nop 1
	v_mov_b32_dpp v8, v4 row_bcast:15 row_mask:0xa bank_mask:0xf
	v_max_f32_e32 v8, v8, v8
	v_max_f32_e32 v4, v4, v8
	v_mov_b32_e32 v8, 0xff800000
	s_nop 1
	v_mov_b32_dpp v8, v4 row_bcast:31 row_mask:0xc bank_mask:0xf
	v_max_f32_e32 v8, v8, v8
	v_max_f32_e32 v4, v4, v8
	v_mov_b32_e32 v8, 0xff800000
	v_readlane_b32 s22, v4, 63
	s_nop 1
	v_cmp_eq_f32_e32 vcc, s22, v1
	s_ff1_i32_b64 s22, vcc
	v_cmp_ne_u32_e32 vcc, s22, v198
	s_nop 1
	v_cndmask_b32_e32 v1, v115, v1, vcc
	v_cndmask_b32_e64 v4, 0, -1, vcc
	s_nop 0
	v_mov_b32_dpp v8, v1 row_shr:1 row_mask:0xf bank_mask:0xf
	v_max_f32_e32 v8, v8, v8
	v_max_f32_e32 v8, v1, v8
	s_nop 1
	v_mov_b32_dpp v9, v8 row_shr:2 row_mask:0xf bank_mask:0xf
	v_max_f32_e32 v9, v9, v9
	v_max_f32_e32 v8, v8, v9
	v_mov_b32_e32 v9, 0xff800000
	s_nop 1
	v_mov_b32_dpp v9, v8 row_shr:4 row_mask:0xf bank_mask:0xf
	v_max_f32_e32 v9, v9, v9
	v_max_f32_e32 v8, v8, v9
	v_mov_b32_e32 v9, 0xff800000
	s_nop 1
	v_mov_b32_dpp v9, v8 row_shr:8 row_mask:0xf bank_mask:0xf
	v_max_f32_e32 v9, v9, v9
	v_max_f32_e32 v8, v8, v9
	v_mov_b32_e32 v9, 0xff800000
	s_nop 1
	v_mov_b32_dpp v9, v8 row_bcast:15 row_mask:0xa bank_mask:0xf
	v_max_f32_e32 v9, v9, v9
	v_max_f32_e32 v8, v8, v9
	v_mov_b32_e32 v9, 0xff800000
	s_nop 1
	v_mov_b32_dpp v9, v8 row_bcast:31 row_mask:0xc bank_mask:0xf
	v_max_f32_e32 v9, v9, v9
	v_max_f32_e32 v8, v8, v9
	v_mov_b32_e32 v9, 0xff800000
	v_readlane_b32 s22, v8, 63
	v_mov_b32_e32 v8, 0xff800000
	s_nop 0
	v_cmp_eq_f32_e32 vcc, s22, v1
	s_ff1_i32_b64 s22, vcc
	v_cmp_eq_u32_e32 vcc, s22, v198
	s_nop 1
	v_cndmask_b32_e32 v1, v1, v115, vcc
	v_cndmask_b32_e64 v4, v4, 1, vcc
	s_nop 0
	v_mov_b32_dpp v8, v1 row_shr:1 row_mask:0xf bank_mask:0xf
	v_max_f32_e32 v8, v8, v8
	v_max_f32_e32 v8, v1, v8
	s_nop 1
	v_mov_b32_dpp v9, v8 row_shr:2 row_mask:0xf bank_mask:0xf
	v_max_f32_e32 v9, v9, v9
	v_max_f32_e32 v8, v8, v9
	v_mov_b32_e32 v9, 0xff800000
	s_nop 1
	v_mov_b32_dpp v9, v8 row_shr:4 row_mask:0xf bank_mask:0xf
	v_max_f32_e32 v9, v9, v9
	v_max_f32_e32 v8, v8, v9
	v_mov_b32_e32 v9, 0xff800000
	s_nop 1
	v_mov_b32_dpp v9, v8 row_shr:8 row_mask:0xf bank_mask:0xf
	v_max_f32_e32 v9, v9, v9
	v_max_f32_e32 v8, v8, v9
	v_mov_b32_e32 v9, 0xff800000
	s_nop 1
	v_mov_b32_dpp v9, v8 row_bcast:15 row_mask:0xa bank_mask:0xf
	v_max_f32_e32 v9, v9, v9
	v_max_f32_e32 v8, v8, v9
	v_mov_b32_e32 v9, 0xff800000
	s_nop 1
	v_mov_b32_dpp v9, v8 row_bcast:31 row_mask:0xc bank_mask:0xf
	v_max_f32_e32 v9, v9, v9
	v_max_f32_e32 v8, v8, v9
	v_mov_b32_e32 v9, 0xff800000
	v_readlane_b32 s22, v8, 63
	v_mov_b32_e32 v8, 0xff800000
	s_nop 0
	v_cmp_eq_f32_e32 vcc, s22, v1
	s_ff1_i32_b64 s22, vcc
	v_cmp_eq_u32_e32 vcc, s22, v198
	s_nop 1
	v_cndmask_b32_e32 v1, v1, v115, vcc
	v_cndmask_b32_e64 v4, v4, 2, vcc
	s_nop 0
	v_mov_b32_dpp v8, v1 row_shr:1 row_mask:0xf bank_mask:0xf
	v_max_f32_e32 v8, v8, v8
	v_max_f32_e32 v8, v1, v8
	s_nop 1
	v_mov_b32_dpp v9, v8 row_shr:2 row_mask:0xf bank_mask:0xf
	v_max_f32_e32 v9, v9, v9
	v_max_f32_e32 v8, v8, v9
	v_mov_b32_e32 v9, 0xff800000
	s_nop 1
	v_mov_b32_dpp v9, v8 row_shr:4 row_mask:0xf bank_mask:0xf
	v_max_f32_e32 v9, v9, v9
	v_max_f32_e32 v8, v8, v9
	v_mov_b32_e32 v9, 0xff800000
	s_nop 1
	v_mov_b32_dpp v9, v8 row_shr:8 row_mask:0xf bank_mask:0xf
	v_max_f32_e32 v9, v9, v9
	v_max_f32_e32 v8, v8, v9
	v_mov_b32_e32 v9, 0xff800000
	s_nop 1
	v_mov_b32_dpp v9, v8 row_bcast:15 row_mask:0xa bank_mask:0xf
	v_max_f32_e32 v9, v9, v9
	v_max_f32_e32 v8, v8, v9
	v_mov_b32_e32 v9, 0xff800000
	s_nop 1
	v_mov_b32_dpp v9, v8 row_bcast:31 row_mask:0xc bank_mask:0xf
	v_max_f32_e32 v9, v9, v9
	v_max_f32_e32 v8, v8, v9
	v_mov_b32_e32 v9, 0xff800000
	v_readlane_b32 s22, v8, 63
	v_mov_b32_e32 v8, 0xff800000
	s_nop 0
	v_cmp_eq_f32_e32 vcc, s22, v1
	s_ff1_i32_b64 s22, vcc
	v_cmp_eq_u32_e32 vcc, s22, v198
	s_nop 1
	v_cndmask_b32_e32 v1, v1, v115, vcc
	v_cndmask_b32_e64 v4, v4, 3, vcc
	s_nop 0
	v_mov_b32_dpp v8, v1 row_shr:1 row_mask:0xf bank_mask:0xf
	v_max_f32_e32 v8, v8, v8
	v_max_f32_e32 v8, v1, v8
	s_nop 1
	v_mov_b32_dpp v9, v8 row_shr:2 row_mask:0xf bank_mask:0xf
	v_max_f32_e32 v9, v9, v9
	v_max_f32_e32 v8, v8, v9
	v_mov_b32_e32 v9, 0xff800000
	s_nop 1
	v_mov_b32_dpp v9, v8 row_shr:4 row_mask:0xf bank_mask:0xf
	v_max_f32_e32 v9, v9, v9
	v_max_f32_e32 v8, v8, v9
	v_mov_b32_e32 v9, 0xff800000
	s_nop 1
	v_mov_b32_dpp v9, v8 row_shr:8 row_mask:0xf bank_mask:0xf
	v_max_f32_e32 v9, v9, v9
	v_max_f32_e32 v8, v8, v9
	v_mov_b32_e32 v9, 0xff800000
	s_nop 1
	v_mov_b32_dpp v9, v8 row_bcast:15 row_mask:0xa bank_mask:0xf
	v_max_f32_e32 v9, v9, v9
	v_max_f32_e32 v8, v8, v9
	v_mov_b32_e32 v9, 0xff800000
	s_nop 1
	v_mov_b32_dpp v9, v8 row_bcast:31 row_mask:0xc bank_mask:0xf
	v_max_f32_e32 v9, v9, v9
	v_max_f32_e32 v8, v8, v9
	s_nop 0
	v_readlane_b32 s22, v8, 63
	v_mov_b32_e32 v8, 0xff800000
	s_nop 0
	v_cmp_eq_f32_e32 vcc, s22, v1
	s_ff1_i32_b64 s22, vcc
	v_cmp_eq_u32_e32 vcc, s22, v198
	s_nop 1
	v_cndmask_b32_e32 v1, v1, v115, vcc
	v_max_f32_e32 v9, v1, v1
	v_cndmask_b32_e64 v4, v4, 4, vcc
	v_mov_b32_dpp v8, v1 row_shr:1 row_mask:0xf bank_mask:0xf
	v_max_f32_e32 v8, v8, v8
	v_max_f32_e32 v8, v9, v8
	v_mov_b32_e32 v9, 0xff800000
	s_nop 1
	v_mov_b32_dpp v9, v8 row_shr:2 row_mask:0xf bank_mask:0xf
	v_max_f32_e32 v9, v9, v9
	v_max_f32_e32 v8, v8, v9
	v_mov_b32_e32 v9, 0xff800000
	s_nop 1
	v_mov_b32_dpp v9, v8 row_shr:4 row_mask:0xf bank_mask:0xf
	v_max_f32_e32 v9, v9, v9
	v_max_f32_e32 v8, v8, v9
	v_mov_b32_e32 v9, 0xff800000
	s_nop 1
	v_mov_b32_dpp v9, v8 row_shr:8 row_mask:0xf bank_mask:0xf
	v_max_f32_e32 v9, v9, v9
	v_max_f32_e32 v8, v8, v9
	v_mov_b32_e32 v9, 0xff800000
	s_nop 1
	v_mov_b32_dpp v9, v8 row_bcast:15 row_mask:0xa bank_mask:0xf
	v_max_f32_e32 v9, v9, v9
	v_max_f32_e32 v8, v8, v9
	v_mov_b32_e32 v9, 0xff800000
	s_nop 1
	v_mov_b32_dpp v9, v8 row_bcast:31 row_mask:0xc bank_mask:0xf
	v_max_f32_e32 v9, v9, v9
	v_max_f32_e32 v8, v8, v9
	s_nop 0
	v_readlane_b32 s22, v8, 63
	v_mov_b32_e32 v8, 0xff800000
	s_nop 0
	v_cmp_eq_f32_e32 vcc, s22, v1
	s_ff1_i32_b64 s22, vcc
	v_cmp_eq_u32_e32 vcc, s22, v198
	s_nop 1
	v_cndmask_b32_e32 v1, v1, v115, vcc
	v_max_f32_e32 v9, v1, v1
	v_cndmask_b32_e64 v4, v4, 5, vcc
	v_mov_b32_dpp v8, v1 row_shr:1 row_mask:0xf bank_mask:0xf
	v_max_f32_e32 v8, v8, v8
	v_max_f32_e32 v8, v9, v8
	v_mov_b32_e32 v9, 0xff800000
	s_nop 1
	v_mov_b32_dpp v9, v8 row_shr:2 row_mask:0xf bank_mask:0xf
	v_max_f32_e32 v9, v9, v9
	v_max_f32_e32 v8, v8, v9
	v_mov_b32_e32 v9, 0xff800000
	s_nop 1
	v_mov_b32_dpp v9, v8 row_shr:4 row_mask:0xf bank_mask:0xf
	v_max_f32_e32 v9, v9, v9
	v_max_f32_e32 v8, v8, v9
	v_mov_b32_e32 v9, 0xff800000
	s_nop 1
	v_mov_b32_dpp v9, v8 row_shr:8 row_mask:0xf bank_mask:0xf
	v_max_f32_e32 v9, v9, v9
	v_max_f32_e32 v8, v8, v9
	v_mov_b32_e32 v9, 0xff800000
	s_nop 1
	v_mov_b32_dpp v9, v8 row_bcast:15 row_mask:0xa bank_mask:0xf
	v_max_f32_e32 v9, v9, v9
	v_max_f32_e32 v8, v8, v9
	v_mov_b32_e32 v9, 0xff800000
	s_nop 1
	v_mov_b32_dpp v9, v8 row_bcast:31 row_mask:0xc bank_mask:0xf
	v_max_f32_e32 v9, v9, v9
	v_max_f32_e32 v8, v8, v9
	s_nop 0
	v_readlane_b32 s22, v8, 63
	v_mov_b32_e32 v8, 0xff800000
	s_nop 0
	v_cmp_eq_f32_e32 vcc, s22, v1
	s_ff1_i32_b64 s22, vcc
	v_cmp_eq_u32_e32 vcc, s22, v198
	s_nop 1
	v_cndmask_b32_e32 v1, v1, v115, vcc
	v_max_f32_e32 v9, v1, v1
	v_cndmask_b32_e64 v4, v4, 6, vcc
	v_mov_b32_dpp v8, v1 row_shr:1 row_mask:0xf bank_mask:0xf
	v_max_f32_e32 v8, v8, v8
	v_max_f32_e32 v8, v9, v8
	v_mov_b32_e32 v9, 0xff800000
	s_nop 1
	v_mov_b32_dpp v9, v8 row_shr:2 row_mask:0xf bank_mask:0xf
	v_max_f32_e32 v9, v9, v9
	v_max_f32_e32 v8, v8, v9
	v_mov_b32_e32 v9, 0xff800000
	s_nop 1
	v_mov_b32_dpp v9, v8 row_shr:4 row_mask:0xf bank_mask:0xf
	v_max_f32_e32 v9, v9, v9
	v_max_f32_e32 v8, v8, v9
	v_mov_b32_e32 v9, 0xff800000
	s_nop 1
	v_mov_b32_dpp v9, v8 row_shr:8 row_mask:0xf bank_mask:0xf
	v_max_f32_e32 v9, v9, v9
	v_max_f32_e32 v8, v8, v9
	v_mov_b32_e32 v9, 0xff800000
	s_nop 1
	v_mov_b32_dpp v9, v8 row_bcast:15 row_mask:0xa bank_mask:0xf
	v_max_f32_e32 v9, v9, v9
	v_max_f32_e32 v8, v8, v9
	v_mov_b32_e32 v9, 0xff800000
	s_nop 1
	v_mov_b32_dpp v9, v8 row_bcast:31 row_mask:0xc bank_mask:0xf
	v_max_f32_e32 v9, v9, v9
	v_max_f32_e32 v8, v8, v9
	s_nop 0
	v_readlane_b32 s22, v8, 63
	s_nop 1
	v_cmp_eq_f32_e32 vcc, s22, v1
	s_ff1_i32_b64 s22, vcc
	v_cmp_ne_u32_e32 vcc, s22, v198
	s_nop 1
	v_cndmask_b32_e32 v8, 7, v4, vcc
	v_cmp_lt_i32_e64 s[22:23], -1, v8
	v_mov_b32_e32 v4, 0
	s_nop 0
	v_cndmask_b32_e64 v1, 0, v7, s[22:23]
	s_nop 1
	v_add_f32_dpp v1, v1, v1 row_shr:1 row_mask:0xf bank_mask:0xf bound_ctrl:1
	s_nop 1
	v_add_f32_dpp v1, v1, v1 row_shr:2 row_mask:0xf bank_mask:0xf bound_ctrl:1
	s_nop 1
	v_add_f32_dpp v1, v1, v1 row_shr:4 row_mask:0xf bank_mask:0xf bound_ctrl:1
	s_nop 1
	v_add_f32_dpp v1, v1, v1 row_shr:8 row_mask:0xf bank_mask:0xf bound_ctrl:1
	s_nop 1
	v_mov_b32_dpp v4, v1 row_bcast:15 row_mask:0xa bank_mask:0xf
	v_add_f32_e32 v1, v1, v4
	v_mov_b32_e32 v4, 0
	s_nop 1
	v_mov_b32_dpp v4, v1 row_bcast:31 row_mask:0xc bank_mask:0xf
	v_add_f32_e32 v1, v1, v4
	s_nop 0
	v_readlane_b32 s43, v1, 63
	v_mov_b32_e32 v1, s35
	s_and_saveexec_b64 s[24:25], s[22:23]
	ds_add_rtn_u32 v1, v101, v116
	s_or_b64 exec, exec, s[24:25]
	ds_read_b32 v4, v119 offset:512
	s_waitcnt lgkmcnt(0)
	v_mul_f32_e32 v4, 0xbfb8aa3b, v4
	v_exp_f32_e32 v4, v4
	s_nop 0
	v_add_f32_e32 v4, 1.0, v4
	v_div_scale_f32 v9, s[24:25], v4, v4, 1.0
	v_rcp_f32_e32 v10, v9
	v_div_scale_f32 v11, vcc, 1.0, v4, 1.0
	v_fma_f32 v12, -v9, v10, 1.0
	v_fmac_f32_e32 v10, v12, v10
	v_mul_f32_e32 v12, v11, v10
	v_fma_f32 v13, -v9, v12, v11
	v_fmac_f32_e32 v12, v13, v10
	v_fma_f32 v9, -v9, v12, v11
	v_div_fmas_f32 v9, v9, v10, v12
	v_div_fixup_f32 v9, v9, v4, 1.0
	v_add_f32_e32 v4, v3, v9
	s_nop 1
	v_mov_b32_dpp v10, v4 quad_perm:[1,0,3,2] row_mask:0xf bank_mask:0xf bound_ctrl:1
	v_max_f32_e32 v10, v10, v10
	v_max_f32_e32 v10, v4, v10
	s_nop 1
	v_mov_b32_dpp v11, v10 quad_perm:[2,3,0,1] row_mask:0xf bank_mask:0xf bound_ctrl:1
	v_max_f32_e32 v11, v11, v11
	v_max_f32_e32 v10, v10, v11
	s_nop 1
	v_mov_b32_dpp v11, v10 row_half_mirror row_mask:0xf bank_mask:0xf bound_ctrl:1
	v_max_f32_e32 v11, v11, v11
	v_max_f32_e32 v10, v10, v11
	v_cmp_eq_f32_e32 vcc, v4, v10
	s_nop 1
	v_and_b32_e32 v11, vcc_hi, v63
	v_and_b32_e32 v12, vcc_lo, v62
	v_ffbl_b32_e32 v11, v11
	v_ffbl_b32_e32 v12, v12
	v_add_u32_e32 v11, 32, v11
	v_min_u32_e32 v11, v12, v11
	v_cmp_ne_u32_e32 vcc, v198, v11
	s_nop 1
	v_cndmask_b32_e32 v11, v115, v4, vcc
	s_nop 1
	v_mov_b32_dpp v12, v11 quad_perm:[1,0,3,2] row_mask:0xf bank_mask:0xf bound_ctrl:1
	v_max_f32_e32 v12, v12, v12
	v_max_f32_e32 v11, v11, v12
	s_nop 1
	v_mov_b32_dpp v12, v11 quad_perm:[2,3,0,1] row_mask:0xf bank_mask:0xf bound_ctrl:1
	v_max_f32_e32 v12, v12, v12
	v_max_f32_e32 v11, v11, v12
	s_nop 1
	v_mov_b32_dpp v12, v11 row_half_mirror row_mask:0xf bank_mask:0xf bound_ctrl:1
	v_max_f32_e32 v12, v12, v12
	v_max_f32_e32 v11, v11, v12
	v_add_f32_e32 v10, v10, v11
	s_nop 0
	v_readlane_b32 s24, v10, 0
	v_readlane_b32 s26, v10, 8
	s_nop 0
	v_cmp_gt_f32_e32 vcc, s24, v10
	v_cmp_eq_f32_e64 s[24:25], s24, v10
	s_and_b64 s[24:25], s[24:25], s[6:7]
	s_or_b64 s[24:25], vcc, s[24:25]
	v_cndmask_b32_e64 v11, 0, 1, s[24:25]
	v_cmp_eq_f32_e64 s[24:25], s26, v10
	v_cmp_gt_f32_e32 vcc, s26, v10
	s_and_b64 s[24:25], s[24:25], s[8:9]
	s_or_b64 s[24:25], vcc, s[24:25]
	v_cndmask_b32_e64 v12, 0, 1, s[24:25]
	v_readlane_b32 s24, v10, 16
	s_nop 1
	v_cmp_gt_f32_e32 vcc, s24, v10
	v_cmp_eq_f32_e64 s[24:25], s24, v10
	s_and_b64 s[24:25], s[24:25], s[10:11]
	s_or_b64 s[24:25], vcc, s[24:25]
	v_cndmask_b32_e64 v13, 0, 1, s[24:25]
	v_readlane_b32 s24, v10, 24
	v_add3_u32 v11, v11, v12, v13
	s_nop 0
	v_cmp_gt_f32_e32 vcc, s24, v10
	v_cmp_eq_f32_e64 s[24:25], s24, v10
	s_and_b64 s[24:25], s[24:25], s[12:13]
	s_or_b64 s[24:25], vcc, s[24:25]
	v_cndmask_b32_e64 v12, 0, 1, s[24:25]
	v_readlane_b32 s24, v10, 32
	s_nop 1
	v_cmp_gt_f32_e32 vcc, s24, v10
	v_cmp_eq_f32_e64 s[24:25], s24, v10
	s_and_b64 s[24:25], s[24:25], s[14:15]
	s_or_b64 s[24:25], vcc, s[24:25]
	v_cndmask_b32_e64 v13, 0, 1, s[24:25]
	v_readlane_b32 s24, v10, 40
	v_add3_u32 v11, v11, v12, v13
	s_nop 0
	v_cmp_gt_f32_e32 vcc, s24, v10
	v_cmp_eq_f32_e64 s[24:25], s24, v10
	s_and_b64 s[24:25], s[24:25], s[16:17]
	s_or_b64 s[24:25], vcc, s[24:25]
	v_cndmask_b32_e64 v12, 0, 1, s[24:25]
	v_readlane_b32 s24, v10, 48
	s_nop 1
	v_cmp_gt_f32_e32 vcc, s24, v10
	v_cmp_eq_f32_e64 s[24:25], s24, v10
	s_and_b64 s[24:25], s[18:19], s[24:25]
	s_or_b64 s[24:25], vcc, s[24:25]
	v_cndmask_b32_e64 v13, 0, 1, s[24:25]
	v_readlane_b32 s24, v10, 56
	s_nop 1
	v_cmp_gt_f32_e32 vcc, s24, v10
	s_nop 1
	v_addc_co_u32_e32 v10, vcc, v11, v12, vcc
	v_add_u32_e32 v10, v10, v13
	v_cmp_gt_u32_e32 vcc, 4, v10
	v_mov_b32_e32 v10, 0xff800000
	v_mov_b32_e32 v11, 0xff800000
	v_cndmask_b32_e32 v4, v115, v4, vcc
	v_mov_b32_e32 v12, 0xff800000
	s_nop 0
	v_mov_b32_dpp v10, v4 row_shr:1 row_mask:0xf bank_mask:0xf
	v_max_f32_e32 v10, v10, v10
	v_max_f32_e32 v10, v4, v10
	s_nop 1
	v_mov_b32_dpp v11, v10 row_shr:2 row_mask:0xf bank_mask:0xf
	v_max_f32_e32 v11, v11, v11
	v_max_f32_e32 v10, v10, v11
	v_mov_b32_e32 v11, 0xff800000
	s_nop 1
	v_mov_b32_dpp v11, v10 row_shr:4 row_mask:0xf bank_mask:0xf
	v_max_f32_e32 v11, v11, v11
	v_max_f32_e32 v10, v10, v11
	v_mov_b32_e32 v11, 0xff800000
	s_nop 1
	v_mov_b32_dpp v11, v10 row_shr:8 row_mask:0xf bank_mask:0xf
	v_max_f32_e32 v11, v11, v11
	v_max_f32_e32 v10, v10, v11
	v_mov_b32_e32 v11, 0xff800000
	s_nop 1
	v_mov_b32_dpp v11, v10 row_bcast:15 row_mask:0xa bank_mask:0xf
	v_max_f32_e32 v11, v11, v11
	v_max_f32_e32 v10, v10, v11
	v_mov_b32_e32 v11, 0xff800000
	s_nop 1
	v_mov_b32_dpp v11, v10 row_bcast:31 row_mask:0xc bank_mask:0xf
	v_max_f32_e32 v11, v11, v11
	v_max_f32_e32 v10, v10, v11
	v_mov_b32_e32 v11, 0xff800000
	v_readlane_b32 s24, v10, 63
	s_nop 1
	v_cmp_eq_f32_e32 vcc, s24, v4
	s_ff1_i32_b64 s24, vcc
	v_cmp_ne_u32_e32 vcc, s24, v198
	s_nop 1
	v_cndmask_b32_e32 v4, v115, v4, vcc
	v_cndmask_b32_e64 v10, 0, -1, vcc
	s_nop 0
	v_mov_b32_dpp v11, v4 row_shr:1 row_mask:0xf bank_mask:0xf
	v_max_f32_e32 v11, v11, v11
	v_max_f32_e32 v11, v4, v11
	s_nop 1
	v_mov_b32_dpp v12, v11 row_shr:2 row_mask:0xf bank_mask:0xf
	v_max_f32_e32 v12, v12, v12
	v_max_f32_e32 v11, v11, v12
	v_mov_b32_e32 v12, 0xff800000
	s_nop 1
	v_mov_b32_dpp v12, v11 row_shr:4 row_mask:0xf bank_mask:0xf
	v_max_f32_e32 v12, v12, v12
	v_max_f32_e32 v11, v11, v12
	v_mov_b32_e32 v12, 0xff800000
	s_nop 1
	v_mov_b32_dpp v12, v11 row_shr:8 row_mask:0xf bank_mask:0xf
	v_max_f32_e32 v12, v12, v12
	v_max_f32_e32 v11, v11, v12
	v_mov_b32_e32 v12, 0xff800000
	s_nop 1
	v_mov_b32_dpp v12, v11 row_bcast:15 row_mask:0xa bank_mask:0xf
	v_max_f32_e32 v12, v12, v12
	v_max_f32_e32 v11, v11, v12
	v_mov_b32_e32 v12, 0xff800000
	s_nop 1
	v_mov_b32_dpp v12, v11 row_bcast:31 row_mask:0xc bank_mask:0xf
	v_max_f32_e32 v12, v12, v12
	v_max_f32_e32 v11, v11, v12
	v_mov_b32_e32 v12, 0xff800000
	v_readlane_b32 s24, v11, 63
	v_mov_b32_e32 v11, 0xff800000
	s_nop 0
	v_cmp_eq_f32_e32 vcc, s24, v4
	s_ff1_i32_b64 s24, vcc
	v_cmp_eq_u32_e32 vcc, s24, v198
	s_nop 1
	v_cndmask_b32_e32 v4, v4, v115, vcc
	v_cndmask_b32_e64 v10, v10, 1, vcc
	s_nop 0
	v_mov_b32_dpp v11, v4 row_shr:1 row_mask:0xf bank_mask:0xf
	v_max_f32_e32 v11, v11, v11
	v_max_f32_e32 v11, v4, v11
	s_nop 1
	v_mov_b32_dpp v12, v11 row_shr:2 row_mask:0xf bank_mask:0xf
	v_max_f32_e32 v12, v12, v12
	v_max_f32_e32 v11, v11, v12
	v_mov_b32_e32 v12, 0xff800000
	s_nop 1
	v_mov_b32_dpp v12, v11 row_shr:4 row_mask:0xf bank_mask:0xf
	v_max_f32_e32 v12, v12, v12
	v_max_f32_e32 v11, v11, v12
	v_mov_b32_e32 v12, 0xff800000
	s_nop 1
	v_mov_b32_dpp v12, v11 row_shr:8 row_mask:0xf bank_mask:0xf
	v_max_f32_e32 v12, v12, v12
	v_max_f32_e32 v11, v11, v12
	v_mov_b32_e32 v12, 0xff800000
	s_nop 1
	v_mov_b32_dpp v12, v11 row_bcast:15 row_mask:0xa bank_mask:0xf
	v_max_f32_e32 v12, v12, v12
	v_max_f32_e32 v11, v11, v12
	v_mov_b32_e32 v12, 0xff800000
	s_nop 1
	v_mov_b32_dpp v12, v11 row_bcast:31 row_mask:0xc bank_mask:0xf
	v_max_f32_e32 v12, v12, v12
	v_max_f32_e32 v11, v11, v12
	v_mov_b32_e32 v12, 0xff800000
	v_readlane_b32 s24, v11, 63
	v_mov_b32_e32 v11, 0xff800000
	s_nop 0
	v_cmp_eq_f32_e32 vcc, s24, v4
	s_ff1_i32_b64 s24, vcc
	v_cmp_eq_u32_e32 vcc, s24, v198
	s_nop 1
	v_cndmask_b32_e32 v4, v4, v115, vcc
	v_cndmask_b32_e64 v10, v10, 2, vcc
	s_nop 0
	v_mov_b32_dpp v11, v4 row_shr:1 row_mask:0xf bank_mask:0xf
	v_max_f32_e32 v11, v11, v11
	v_max_f32_e32 v11, v4, v11
	s_nop 1
	v_mov_b32_dpp v12, v11 row_shr:2 row_mask:0xf bank_mask:0xf
	v_max_f32_e32 v12, v12, v12
	v_max_f32_e32 v11, v11, v12
	v_mov_b32_e32 v12, 0xff800000
	s_nop 1
	v_mov_b32_dpp v12, v11 row_shr:4 row_mask:0xf bank_mask:0xf
	v_max_f32_e32 v12, v12, v12
	v_max_f32_e32 v11, v11, v12
	v_mov_b32_e32 v12, 0xff800000
	s_nop 1
	v_mov_b32_dpp v12, v11 row_shr:8 row_mask:0xf bank_mask:0xf
	v_max_f32_e32 v12, v12, v12
	v_max_f32_e32 v11, v11, v12
	v_mov_b32_e32 v12, 0xff800000
	s_nop 1
	v_mov_b32_dpp v12, v11 row_bcast:15 row_mask:0xa bank_mask:0xf
	v_max_f32_e32 v12, v12, v12
	v_max_f32_e32 v11, v11, v12
	v_mov_b32_e32 v12, 0xff800000
	s_nop 1
	v_mov_b32_dpp v12, v11 row_bcast:31 row_mask:0xc bank_mask:0xf
	v_max_f32_e32 v12, v12, v12
	v_max_f32_e32 v11, v11, v12
	v_mov_b32_e32 v12, 0xff800000
	v_readlane_b32 s24, v11, 63
	v_mov_b32_e32 v11, 0xff800000
	s_nop 0
	v_cmp_eq_f32_e32 vcc, s24, v4
	s_ff1_i32_b64 s24, vcc
	v_cmp_eq_u32_e32 vcc, s24, v198
	s_nop 1
	v_cndmask_b32_e32 v4, v4, v115, vcc
	v_cndmask_b32_e64 v10, v10, 3, vcc
	s_nop 0
	v_mov_b32_dpp v11, v4 row_shr:1 row_mask:0xf bank_mask:0xf
	v_max_f32_e32 v11, v11, v11
	v_max_f32_e32 v11, v4, v11
	s_nop 1
	v_mov_b32_dpp v12, v11 row_shr:2 row_mask:0xf bank_mask:0xf
	v_max_f32_e32 v12, v12, v12
	v_max_f32_e32 v11, v11, v12
	v_mov_b32_e32 v12, 0xff800000
	s_nop 1
	v_mov_b32_dpp v12, v11 row_shr:4 row_mask:0xf bank_mask:0xf
	v_max_f32_e32 v12, v12, v12
	v_max_f32_e32 v11, v11, v12
	v_mov_b32_e32 v12, 0xff800000
	s_nop 1
	v_mov_b32_dpp v12, v11 row_shr:8 row_mask:0xf bank_mask:0xf
	v_max_f32_e32 v12, v12, v12
	v_max_f32_e32 v11, v11, v12
	v_mov_b32_e32 v12, 0xff800000
	s_nop 1
	v_mov_b32_dpp v12, v11 row_bcast:15 row_mask:0xa bank_mask:0xf
	v_max_f32_e32 v12, v12, v12
	v_max_f32_e32 v11, v11, v12
	v_mov_b32_e32 v12, 0xff800000
	s_nop 1
	v_mov_b32_dpp v12, v11 row_bcast:31 row_mask:0xc bank_mask:0xf
	v_max_f32_e32 v12, v12, v12
	v_max_f32_e32 v11, v11, v12
	s_nop 0
	v_readlane_b32 s24, v11, 63
	v_mov_b32_e32 v11, 0xff800000
	s_nop 0
	v_cmp_eq_f32_e32 vcc, s24, v4
	s_ff1_i32_b64 s24, vcc
	v_cmp_eq_u32_e32 vcc, s24, v198
	s_nop 1
	v_cndmask_b32_e32 v4, v4, v115, vcc
	v_max_f32_e32 v12, v4, v4
	v_cndmask_b32_e64 v10, v10, 4, vcc
	v_mov_b32_dpp v11, v4 row_shr:1 row_mask:0xf bank_mask:0xf
	v_max_f32_e32 v11, v11, v11
	v_max_f32_e32 v11, v12, v11
	v_mov_b32_e32 v12, 0xff800000
	s_nop 1
	v_mov_b32_dpp v12, v11 row_shr:2 row_mask:0xf bank_mask:0xf
	v_max_f32_e32 v12, v12, v12
	v_max_f32_e32 v11, v11, v12
	v_mov_b32_e32 v12, 0xff800000
	s_nop 1
	v_mov_b32_dpp v12, v11 row_shr:4 row_mask:0xf bank_mask:0xf
	v_max_f32_e32 v12, v12, v12
	v_max_f32_e32 v11, v11, v12
	v_mov_b32_e32 v12, 0xff800000
	s_nop 1
	v_mov_b32_dpp v12, v11 row_shr:8 row_mask:0xf bank_mask:0xf
	v_max_f32_e32 v12, v12, v12
	v_max_f32_e32 v11, v11, v12
	v_mov_b32_e32 v12, 0xff800000
	s_nop 1
	v_mov_b32_dpp v12, v11 row_bcast:15 row_mask:0xa bank_mask:0xf
	v_max_f32_e32 v12, v12, v12
	v_max_f32_e32 v11, v11, v12
	v_mov_b32_e32 v12, 0xff800000
	s_nop 1
	v_mov_b32_dpp v12, v11 row_bcast:31 row_mask:0xc bank_mask:0xf
	v_max_f32_e32 v12, v12, v12
	v_max_f32_e32 v11, v11, v12
	s_nop 0
	v_readlane_b32 s24, v11, 63
	v_mov_b32_e32 v11, 0xff800000
	s_nop 0
	v_cmp_eq_f32_e32 vcc, s24, v4
	s_ff1_i32_b64 s24, vcc
	v_cmp_eq_u32_e32 vcc, s24, v198
	s_nop 1
	v_cndmask_b32_e32 v4, v4, v115, vcc
	v_max_f32_e32 v12, v4, v4
	v_cndmask_b32_e64 v10, v10, 5, vcc
	v_mov_b32_dpp v11, v4 row_shr:1 row_mask:0xf bank_mask:0xf
	v_max_f32_e32 v11, v11, v11
	v_max_f32_e32 v11, v12, v11
	v_mov_b32_e32 v12, 0xff800000
	s_nop 1
	v_mov_b32_dpp v12, v11 row_shr:2 row_mask:0xf bank_mask:0xf
	v_max_f32_e32 v12, v12, v12
	v_max_f32_e32 v11, v11, v12
	v_mov_b32_e32 v12, 0xff800000
	s_nop 1
	v_mov_b32_dpp v12, v11 row_shr:4 row_mask:0xf bank_mask:0xf
	v_max_f32_e32 v12, v12, v12
	v_max_f32_e32 v11, v11, v12
	v_mov_b32_e32 v12, 0xff800000
	s_nop 1
	v_mov_b32_dpp v12, v11 row_shr:8 row_mask:0xf bank_mask:0xf
	v_max_f32_e32 v12, v12, v12
	v_max_f32_e32 v11, v11, v12
	v_mov_b32_e32 v12, 0xff800000
	s_nop 1
	v_mov_b32_dpp v12, v11 row_bcast:15 row_mask:0xa bank_mask:0xf
	v_max_f32_e32 v12, v12, v12
	v_max_f32_e32 v11, v11, v12
	v_mov_b32_e32 v12, 0xff800000
	s_nop 1
	v_mov_b32_dpp v12, v11 row_bcast:31 row_mask:0xc bank_mask:0xf
	v_max_f32_e32 v12, v12, v12
	v_max_f32_e32 v11, v11, v12
	s_nop 0
	v_readlane_b32 s24, v11, 63
	v_mov_b32_e32 v11, 0xff800000
	s_nop 0
	v_cmp_eq_f32_e32 vcc, s24, v4
	s_ff1_i32_b64 s24, vcc
	v_cmp_eq_u32_e32 vcc, s24, v198
	s_nop 1
	v_cndmask_b32_e32 v4, v4, v115, vcc
	v_max_f32_e32 v12, v4, v4
	v_cndmask_b32_e64 v10, v10, 6, vcc
	v_mov_b32_dpp v11, v4 row_shr:1 row_mask:0xf bank_mask:0xf
	v_max_f32_e32 v11, v11, v11
	v_max_f32_e32 v11, v12, v11
	v_mov_b32_e32 v12, 0xff800000
	s_nop 1
	v_mov_b32_dpp v12, v11 row_shr:2 row_mask:0xf bank_mask:0xf
	v_max_f32_e32 v12, v12, v12
	v_max_f32_e32 v11, v11, v12
	v_mov_b32_e32 v12, 0xff800000
	s_nop 1
	v_mov_b32_dpp v12, v11 row_shr:4 row_mask:0xf bank_mask:0xf
	v_max_f32_e32 v12, v12, v12
	v_max_f32_e32 v11, v11, v12
	v_mov_b32_e32 v12, 0xff800000
	s_nop 1
	v_mov_b32_dpp v12, v11 row_shr:8 row_mask:0xf bank_mask:0xf
	v_max_f32_e32 v12, v12, v12
	v_max_f32_e32 v11, v11, v12
	v_mov_b32_e32 v12, 0xff800000
	s_nop 1
	v_mov_b32_dpp v12, v11 row_bcast:15 row_mask:0xa bank_mask:0xf
	v_max_f32_e32 v12, v12, v12
	v_max_f32_e32 v11, v11, v12
	v_mov_b32_e32 v12, 0xff800000
	s_nop 1
	v_mov_b32_dpp v12, v11 row_bcast:31 row_mask:0xc bank_mask:0xf
	v_max_f32_e32 v12, v12, v12
	v_max_f32_e32 v11, v11, v12
	s_nop 0
	v_readlane_b32 s24, v11, 63
	v_mov_b32_e32 v11, 0
	s_nop 0
	v_cmp_eq_f32_e32 vcc, s24, v4
	s_ff1_i32_b64 s24, vcc
	v_cmp_ne_u32_e32 vcc, s24, v198
	s_nop 1
	v_cndmask_b32_e32 v10, 7, v10, vcc
	v_cmp_lt_i32_e64 s[24:25], -1, v10
	s_nop 1
	v_cndmask_b32_e64 v4, 0, v9, s[24:25]
	s_nop 1
	v_add_f32_dpp v4, v4, v4 row_shr:1 row_mask:0xf bank_mask:0xf bound_ctrl:1
	s_nop 1
	v_add_f32_dpp v4, v4, v4 row_shr:2 row_mask:0xf bank_mask:0xf bound_ctrl:1
	s_nop 1
	v_add_f32_dpp v4, v4, v4 row_shr:4 row_mask:0xf bank_mask:0xf bound_ctrl:1
	s_nop 1
	v_add_f32_dpp v4, v4, v4 row_shr:8 row_mask:0xf bank_mask:0xf bound_ctrl:1
	s_nop 1
	v_mov_b32_dpp v11, v4 row_bcast:15 row_mask:0xa bank_mask:0xf
	v_add_f32_e32 v4, v4, v11
	v_mov_b32_e32 v11, 0
	s_nop 1
	v_mov_b32_dpp v11, v4 row_bcast:31 row_mask:0xc bank_mask:0xf
	v_add_f32_e32 v4, v4, v11
	s_nop 0
	v_readlane_b32 s45, v4, 63
	v_mov_b32_e32 v4, s35
	s_and_saveexec_b64 s[26:27], s[24:25]
	ds_add_rtn_u32 v4, v101, v116
	s_or_b64 exec, exec, s[26:27]
	ds_read_b32 v11, v119 offset:768
	s_waitcnt lgkmcnt(0)
	v_mul_f32_e32 v11, 0xbfb8aa3b, v11
	v_exp_f32_e32 v11, v11
	s_nop 0
	v_add_f32_e32 v11, 1.0, v11
	v_div_scale_f32 v12, s[26:27], v11, v11, 1.0
	v_rcp_f32_e32 v13, v12
	v_div_scale_f32 v14, vcc, 1.0, v11, 1.0
	v_fma_f32 v15, -v12, v13, 1.0
	v_fmac_f32_e32 v13, v15, v13
	v_mul_f32_e32 v15, v14, v13
	v_fma_f32 v16, -v12, v15, v14
	v_fmac_f32_e32 v15, v16, v13
	v_fma_f32 v12, -v12, v15, v14
	v_div_fmas_f32 v12, v12, v13, v15
	v_div_fixup_f32 v11, v12, v11, 1.0
	v_add_f32_e32 v3, v3, v11
	s_nop 1
	v_mov_b32_dpp v12, v3 quad_perm:[1,0,3,2] row_mask:0xf bank_mask:0xf bound_ctrl:1
	v_max_f32_e32 v12, v12, v12
	v_max_f32_e32 v12, v3, v12
	s_nop 1
	v_mov_b32_dpp v13, v12 quad_perm:[2,3,0,1] row_mask:0xf bank_mask:0xf bound_ctrl:1
	v_max_f32_e32 v13, v13, v13
	v_max_f32_e32 v12, v12, v13
	s_nop 1
	v_mov_b32_dpp v13, v12 row_half_mirror row_mask:0xf bank_mask:0xf bound_ctrl:1
	v_max_f32_e32 v13, v13, v13
	v_max_f32_e32 v12, v12, v13
	v_cmp_eq_f32_e32 vcc, v3, v12
	s_nop 1
	v_and_b32_e32 v13, vcc_hi, v63
	v_and_b32_e32 v14, vcc_lo, v62
	v_ffbl_b32_e32 v13, v13
	v_ffbl_b32_e32 v14, v14
	v_add_u32_e32 v13, 32, v13
	v_min_u32_e32 v13, v14, v13
	v_cmp_ne_u32_e32 vcc, v198, v13
	s_nop 1
	v_cndmask_b32_e32 v13, v115, v3, vcc
	s_nop 1
	v_mov_b32_dpp v14, v13 quad_perm:[1,0,3,2] row_mask:0xf bank_mask:0xf bound_ctrl:1
	v_max_f32_e32 v14, v14, v14
	v_max_f32_e32 v13, v13, v14
	s_nop 1
	v_mov_b32_dpp v14, v13 quad_perm:[2,3,0,1] row_mask:0xf bank_mask:0xf bound_ctrl:1
	v_max_f32_e32 v14, v14, v14
	v_max_f32_e32 v13, v13, v14
	s_nop 1
	v_mov_b32_dpp v14, v13 row_half_mirror row_mask:0xf bank_mask:0xf bound_ctrl:1
	v_max_f32_e32 v14, v14, v14
	v_max_f32_e32 v13, v13, v14
	v_add_f32_e32 v12, v12, v13
	s_nop 0
	v_readlane_b32 s26, v12, 0
	v_readlane_b32 s47, v12, 8
	s_nop 0
	v_cmp_gt_f32_e32 vcc, s26, v12
	v_cmp_eq_f32_e64 s[26:27], s26, v12
	s_and_b64 s[26:27], s[26:27], s[6:7]
	s_or_b64 s[26:27], vcc, s[26:27]
	v_cndmask_b32_e64 v13, 0, 1, s[26:27]
	v_cmp_eq_f32_e64 s[26:27], s47, v12
	v_cmp_gt_f32_e32 vcc, s47, v12
	s_and_b64 s[26:27], s[26:27], s[8:9]
	s_or_b64 s[26:27], vcc, s[26:27]
	v_cndmask_b32_e64 v14, 0, 1, s[26:27]
	v_readlane_b32 s26, v12, 16
	s_nop 1
	v_cmp_gt_f32_e32 vcc, s26, v12
	v_cmp_eq_f32_e64 s[26:27], s26, v12
	s_and_b64 s[26:27], s[26:27], s[10:11]
	s_or_b64 s[26:27], vcc, s[26:27]
	v_cndmask_b32_e64 v15, 0, 1, s[26:27]
	v_readlane_b32 s26, v12, 24
	v_add3_u32 v13, v13, v14, v15
	s_nop 0
	v_cmp_gt_f32_e32 vcc, s26, v12
	v_cmp_eq_f32_e64 s[26:27], s26, v12
	s_and_b64 s[26:27], s[26:27], s[12:13]
	s_or_b64 s[26:27], vcc, s[26:27]
	v_cndmask_b32_e64 v14, 0, 1, s[26:27]
	v_readlane_b32 s26, v12, 32
	s_nop 1
	v_cmp_gt_f32_e32 vcc, s26, v12
	v_cmp_eq_f32_e64 s[26:27], s26, v12
	s_and_b64 s[26:27], s[26:27], s[14:15]
	s_or_b64 s[26:27], vcc, s[26:27]
	v_cndmask_b32_e64 v15, 0, 1, s[26:27]
	v_readlane_b32 s26, v12, 40
	v_add3_u32 v13, v13, v14, v15
	s_nop 0
	v_cmp_gt_f32_e32 vcc, s26, v12
	v_cmp_eq_f32_e64 s[26:27], s26, v12
	s_and_b64 s[26:27], s[26:27], s[16:17]
	s_or_b64 s[26:27], vcc, s[26:27]
	v_cndmask_b32_e64 v14, 0, 1, s[26:27]
	v_readlane_b32 s26, v12, 48
	s_nop 1
	v_cmp_gt_f32_e32 vcc, s26, v12
	v_cmp_eq_f32_e64 s[26:27], s26, v12
	s_and_b64 s[26:27], s[18:19], s[26:27]
	s_or_b64 s[26:27], vcc, s[26:27]
	v_cndmask_b32_e64 v15, 0, 1, s[26:27]
	v_readlane_b32 s26, v12, 56
	s_nop 1
	v_cmp_gt_f32_e32 vcc, s26, v12
	s_nop 1
	v_addc_co_u32_e32 v12, vcc, v13, v14, vcc
	v_add_u32_e32 v12, v12, v15
	v_cmp_gt_u32_e32 vcc, 4, v12
	v_mov_b32_e32 v12, 0xff800000
	v_mov_b32_e32 v13, 0xff800000
	v_cndmask_b32_e32 v3, v115, v3, vcc
	v_mov_b32_e32 v14, 0xff800000
	s_nop 0
	v_mov_b32_dpp v12, v3 row_shr:1 row_mask:0xf bank_mask:0xf
	v_max_f32_e32 v12, v12, v12
	v_max_f32_e32 v12, v3, v12
	s_nop 1
	v_mov_b32_dpp v13, v12 row_shr:2 row_mask:0xf bank_mask:0xf
	v_max_f32_e32 v13, v13, v13
	v_max_f32_e32 v12, v12, v13
	v_mov_b32_e32 v13, 0xff800000
	s_nop 1
	v_mov_b32_dpp v13, v12 row_shr:4 row_mask:0xf bank_mask:0xf
	v_max_f32_e32 v13, v13, v13
	v_max_f32_e32 v12, v12, v13
	v_mov_b32_e32 v13, 0xff800000
	s_nop 1
	v_mov_b32_dpp v13, v12 row_shr:8 row_mask:0xf bank_mask:0xf
	v_max_f32_e32 v13, v13, v13
	v_max_f32_e32 v12, v12, v13
	v_mov_b32_e32 v13, 0xff800000
	s_nop 1
	v_mov_b32_dpp v13, v12 row_bcast:15 row_mask:0xa bank_mask:0xf
	v_max_f32_e32 v13, v13, v13
	v_max_f32_e32 v12, v12, v13
	v_mov_b32_e32 v13, 0xff800000
	s_nop 1
	v_mov_b32_dpp v13, v12 row_bcast:31 row_mask:0xc bank_mask:0xf
	v_max_f32_e32 v13, v13, v13
	v_max_f32_e32 v12, v12, v13
	v_mov_b32_e32 v13, 0xff800000
	v_readlane_b32 s26, v12, 63
	s_nop 1
	v_cmp_eq_f32_e32 vcc, s26, v3
	s_ff1_i32_b64 s26, vcc
	v_cmp_ne_u32_e32 vcc, s26, v198
	s_nop 1
	v_cndmask_b32_e32 v3, v115, v3, vcc
	v_cndmask_b32_e64 v12, 0, -1, vcc
	s_nop 0
	v_mov_b32_dpp v13, v3 row_shr:1 row_mask:0xf bank_mask:0xf
	v_max_f32_e32 v13, v13, v13
	v_max_f32_e32 v13, v3, v13
	s_nop 1
	v_mov_b32_dpp v14, v13 row_shr:2 row_mask:0xf bank_mask:0xf
	v_max_f32_e32 v14, v14, v14
	v_max_f32_e32 v13, v13, v14
	v_mov_b32_e32 v14, 0xff800000
	s_nop 1
	v_mov_b32_dpp v14, v13 row_shr:4 row_mask:0xf bank_mask:0xf
	v_max_f32_e32 v14, v14, v14
	v_max_f32_e32 v13, v13, v14
	v_mov_b32_e32 v14, 0xff800000
	s_nop 1
	v_mov_b32_dpp v14, v13 row_shr:8 row_mask:0xf bank_mask:0xf
	v_max_f32_e32 v14, v14, v14
	v_max_f32_e32 v13, v13, v14
	v_mov_b32_e32 v14, 0xff800000
	s_nop 1
	v_mov_b32_dpp v14, v13 row_bcast:15 row_mask:0xa bank_mask:0xf
	v_max_f32_e32 v14, v14, v14
	v_max_f32_e32 v13, v13, v14
	v_mov_b32_e32 v14, 0xff800000
	s_nop 1
	v_mov_b32_dpp v14, v13 row_bcast:31 row_mask:0xc bank_mask:0xf
	v_max_f32_e32 v14, v14, v14
	v_max_f32_e32 v13, v13, v14
	v_mov_b32_e32 v14, 0xff800000
	v_readlane_b32 s26, v13, 63
	v_mov_b32_e32 v13, 0xff800000
	s_nop 0
	v_cmp_eq_f32_e32 vcc, s26, v3
	s_ff1_i32_b64 s26, vcc
	v_cmp_eq_u32_e32 vcc, s26, v198
	s_nop 1
	v_cndmask_b32_e32 v3, v3, v115, vcc
	v_cndmask_b32_e64 v12, v12, 1, vcc
	s_nop 0
	v_mov_b32_dpp v13, v3 row_shr:1 row_mask:0xf bank_mask:0xf
	v_max_f32_e32 v13, v13, v13
	v_max_f32_e32 v13, v3, v13
	s_nop 1
	v_mov_b32_dpp v14, v13 row_shr:2 row_mask:0xf bank_mask:0xf
	v_max_f32_e32 v14, v14, v14
	v_max_f32_e32 v13, v13, v14
	v_mov_b32_e32 v14, 0xff800000
	s_nop 1
	v_mov_b32_dpp v14, v13 row_shr:4 row_mask:0xf bank_mask:0xf
	v_max_f32_e32 v14, v14, v14
	v_max_f32_e32 v13, v13, v14
	v_mov_b32_e32 v14, 0xff800000
	s_nop 1
	v_mov_b32_dpp v14, v13 row_shr:8 row_mask:0xf bank_mask:0xf
	v_max_f32_e32 v14, v14, v14
	v_max_f32_e32 v13, v13, v14
	v_mov_b32_e32 v14, 0xff800000
	s_nop 1
	v_mov_b32_dpp v14, v13 row_bcast:15 row_mask:0xa bank_mask:0xf
	v_max_f32_e32 v14, v14, v14
	v_max_f32_e32 v13, v13, v14
	v_mov_b32_e32 v14, 0xff800000
	s_nop 1
	v_mov_b32_dpp v14, v13 row_bcast:31 row_mask:0xc bank_mask:0xf
	v_max_f32_e32 v14, v14, v14
	v_max_f32_e32 v13, v13, v14
	v_mov_b32_e32 v14, 0xff800000
	v_readlane_b32 s26, v13, 63
	v_mov_b32_e32 v13, 0xff800000
	s_nop 0
	v_cmp_eq_f32_e32 vcc, s26, v3
	s_ff1_i32_b64 s26, vcc
	v_cmp_eq_u32_e32 vcc, s26, v198
	s_nop 1
	v_cndmask_b32_e32 v3, v3, v115, vcc
	v_cndmask_b32_e64 v12, v12, 2, vcc
	s_nop 0
	v_mov_b32_dpp v13, v3 row_shr:1 row_mask:0xf bank_mask:0xf
	v_max_f32_e32 v13, v13, v13
	v_max_f32_e32 v13, v3, v13
	s_nop 1
	v_mov_b32_dpp v14, v13 row_shr:2 row_mask:0xf bank_mask:0xf
	v_max_f32_e32 v14, v14, v14
	v_max_f32_e32 v13, v13, v14
	v_mov_b32_e32 v14, 0xff800000
	s_nop 1
	v_mov_b32_dpp v14, v13 row_shr:4 row_mask:0xf bank_mask:0xf
	v_max_f32_e32 v14, v14, v14
	v_max_f32_e32 v13, v13, v14
	v_mov_b32_e32 v14, 0xff800000
	s_nop 1
	v_mov_b32_dpp v14, v13 row_shr:8 row_mask:0xf bank_mask:0xf
	v_max_f32_e32 v14, v14, v14
	v_max_f32_e32 v13, v13, v14
	v_mov_b32_e32 v14, 0xff800000
	s_nop 1
	v_mov_b32_dpp v14, v13 row_bcast:15 row_mask:0xa bank_mask:0xf
	v_max_f32_e32 v14, v14, v14
	v_max_f32_e32 v13, v13, v14
	v_mov_b32_e32 v14, 0xff800000
	s_nop 1
	v_mov_b32_dpp v14, v13 row_bcast:31 row_mask:0xc bank_mask:0xf
	v_max_f32_e32 v14, v14, v14
	v_max_f32_e32 v13, v13, v14
	v_mov_b32_e32 v14, 0xff800000
	v_readlane_b32 s26, v13, 63
	v_mov_b32_e32 v13, 0xff800000
	s_nop 0
	v_cmp_eq_f32_e32 vcc, s26, v3
	s_ff1_i32_b64 s26, vcc
	v_cmp_eq_u32_e32 vcc, s26, v198
	s_nop 1
	v_cndmask_b32_e32 v3, v3, v115, vcc
	v_cndmask_b32_e64 v12, v12, 3, vcc
	s_nop 0
	v_mov_b32_dpp v13, v3 row_shr:1 row_mask:0xf bank_mask:0xf
	v_max_f32_e32 v13, v13, v13
	v_max_f32_e32 v13, v3, v13
	s_nop 1
	v_mov_b32_dpp v14, v13 row_shr:2 row_mask:0xf bank_mask:0xf
	v_max_f32_e32 v14, v14, v14
	v_max_f32_e32 v13, v13, v14
	v_mov_b32_e32 v14, 0xff800000
	s_nop 1
	v_mov_b32_dpp v14, v13 row_shr:4 row_mask:0xf bank_mask:0xf
	v_max_f32_e32 v14, v14, v14
	v_max_f32_e32 v13, v13, v14
	v_mov_b32_e32 v14, 0xff800000
	s_nop 1
	v_mov_b32_dpp v14, v13 row_shr:8 row_mask:0xf bank_mask:0xf
	v_max_f32_e32 v14, v14, v14
	v_max_f32_e32 v13, v13, v14
	v_mov_b32_e32 v14, 0xff800000
	s_nop 1
	v_mov_b32_dpp v14, v13 row_bcast:15 row_mask:0xa bank_mask:0xf
	v_max_f32_e32 v14, v14, v14
	v_max_f32_e32 v13, v13, v14
	v_mov_b32_e32 v14, 0xff800000
	s_nop 1
	v_mov_b32_dpp v14, v13 row_bcast:31 row_mask:0xc bank_mask:0xf
	v_max_f32_e32 v14, v14, v14
	v_max_f32_e32 v13, v13, v14
	s_nop 0
	v_readlane_b32 s26, v13, 63
	v_mov_b32_e32 v13, 0xff800000
	s_nop 0
	v_cmp_eq_f32_e32 vcc, s26, v3
	s_ff1_i32_b64 s26, vcc
	v_cmp_eq_u32_e32 vcc, s26, v198
	s_nop 1
	v_cndmask_b32_e32 v3, v3, v115, vcc
	v_max_f32_e32 v14, v3, v3
	v_cndmask_b32_e64 v12, v12, 4, vcc
	v_mov_b32_dpp v13, v3 row_shr:1 row_mask:0xf bank_mask:0xf
	v_max_f32_e32 v13, v13, v13
	v_max_f32_e32 v13, v14, v13
	v_mov_b32_e32 v14, 0xff800000
	s_nop 1
	v_mov_b32_dpp v14, v13 row_shr:2 row_mask:0xf bank_mask:0xf
	v_max_f32_e32 v14, v14, v14
	v_max_f32_e32 v13, v13, v14
	v_mov_b32_e32 v14, 0xff800000
	s_nop 1
	v_mov_b32_dpp v14, v13 row_shr:4 row_mask:0xf bank_mask:0xf
	v_max_f32_e32 v14, v14, v14
	v_max_f32_e32 v13, v13, v14
	v_mov_b32_e32 v14, 0xff800000
	s_nop 1
	v_mov_b32_dpp v14, v13 row_shr:8 row_mask:0xf bank_mask:0xf
	v_max_f32_e32 v14, v14, v14
	v_max_f32_e32 v13, v13, v14
	v_mov_b32_e32 v14, 0xff800000
	s_nop 1
	v_mov_b32_dpp v14, v13 row_bcast:15 row_mask:0xa bank_mask:0xf
	v_max_f32_e32 v14, v14, v14
	v_max_f32_e32 v13, v13, v14
	v_mov_b32_e32 v14, 0xff800000
	s_nop 1
	v_mov_b32_dpp v14, v13 row_bcast:31 row_mask:0xc bank_mask:0xf
	v_max_f32_e32 v14, v14, v14
	v_max_f32_e32 v13, v13, v14
	s_nop 0
	v_readlane_b32 s26, v13, 63
	v_mov_b32_e32 v13, 0xff800000
	s_nop 0
	v_cmp_eq_f32_e32 vcc, s26, v3
	s_ff1_i32_b64 s26, vcc
	v_cmp_eq_u32_e32 vcc, s26, v198
	s_nop 1
	v_cndmask_b32_e32 v3, v3, v115, vcc
	v_max_f32_e32 v14, v3, v3
	v_cndmask_b32_e64 v12, v12, 5, vcc
	v_mov_b32_dpp v13, v3 row_shr:1 row_mask:0xf bank_mask:0xf
	v_max_f32_e32 v13, v13, v13
	v_max_f32_e32 v13, v14, v13
	v_mov_b32_e32 v14, 0xff800000
	s_nop 1
	v_mov_b32_dpp v14, v13 row_shr:2 row_mask:0xf bank_mask:0xf
	v_max_f32_e32 v14, v14, v14
	v_max_f32_e32 v13, v13, v14
	v_mov_b32_e32 v14, 0xff800000
	s_nop 1
	v_mov_b32_dpp v14, v13 row_shr:4 row_mask:0xf bank_mask:0xf
	v_max_f32_e32 v14, v14, v14
	v_max_f32_e32 v13, v13, v14
	v_mov_b32_e32 v14, 0xff800000
	s_nop 1
	v_mov_b32_dpp v14, v13 row_shr:8 row_mask:0xf bank_mask:0xf
	v_max_f32_e32 v14, v14, v14
	v_max_f32_e32 v13, v13, v14
	v_mov_b32_e32 v14, 0xff800000
	s_nop 1
	v_mov_b32_dpp v14, v13 row_bcast:15 row_mask:0xa bank_mask:0xf
	v_max_f32_e32 v14, v14, v14
	v_max_f32_e32 v13, v13, v14
	v_mov_b32_e32 v14, 0xff800000
	s_nop 1
	v_mov_b32_dpp v14, v13 row_bcast:31 row_mask:0xc bank_mask:0xf
	v_max_f32_e32 v14, v14, v14
	v_max_f32_e32 v13, v13, v14
	s_nop 0
	v_readlane_b32 s26, v13, 63
	v_mov_b32_e32 v13, 0xff800000
	s_nop 0
	v_cmp_eq_f32_e32 vcc, s26, v3
	s_ff1_i32_b64 s26, vcc
	v_cmp_eq_u32_e32 vcc, s26, v198
	s_nop 1
	v_cndmask_b32_e32 v3, v3, v115, vcc
	v_max_f32_e32 v14, v3, v3
	v_cndmask_b32_e64 v12, v12, 6, vcc
	v_mov_b32_dpp v13, v3 row_shr:1 row_mask:0xf bank_mask:0xf
	v_max_f32_e32 v13, v13, v13
	v_max_f32_e32 v13, v14, v13
	v_mov_b32_e32 v14, 0xff800000
	s_nop 1
	v_mov_b32_dpp v14, v13 row_shr:2 row_mask:0xf bank_mask:0xf
	v_max_f32_e32 v14, v14, v14
	v_max_f32_e32 v13, v13, v14
	v_mov_b32_e32 v14, 0xff800000
	s_nop 1
	v_mov_b32_dpp v14, v13 row_shr:4 row_mask:0xf bank_mask:0xf
	v_max_f32_e32 v14, v14, v14
	v_max_f32_e32 v13, v13, v14
	v_mov_b32_e32 v14, 0xff800000
	s_nop 1
	v_mov_b32_dpp v14, v13 row_shr:8 row_mask:0xf bank_mask:0xf
	v_max_f32_e32 v14, v14, v14
	v_max_f32_e32 v13, v13, v14
	v_mov_b32_e32 v14, 0xff800000
	s_nop 1
	v_mov_b32_dpp v14, v13 row_bcast:15 row_mask:0xa bank_mask:0xf
	v_max_f32_e32 v14, v14, v14
	v_max_f32_e32 v13, v13, v14
	v_mov_b32_e32 v14, 0xff800000
	s_nop 1
	v_mov_b32_dpp v14, v13 row_bcast:31 row_mask:0xc bank_mask:0xf
	v_max_f32_e32 v14, v14, v14
	v_max_f32_e32 v13, v13, v14
	s_nop 0
	v_readlane_b32 s26, v13, 63
	v_mov_b32_e32 v13, 0
	s_nop 0
	v_cmp_eq_f32_e32 vcc, s26, v3
	s_ff1_i32_b64 s26, vcc
	v_cmp_ne_u32_e32 vcc, s26, v198
	s_nop 1
	v_cndmask_b32_e32 v12, 7, v12, vcc
	v_cmp_lt_i32_e64 s[26:27], -1, v12
	s_nop 1
	v_cndmask_b32_e64 v3, 0, v11, s[26:27]
	s_nop 1
	v_add_f32_dpp v3, v3, v3 row_shr:1 row_mask:0xf bank_mask:0xf bound_ctrl:1
	s_nop 1
	v_add_f32_dpp v3, v3, v3 row_shr:2 row_mask:0xf bank_mask:0xf bound_ctrl:1
	s_nop 1
	v_add_f32_dpp v3, v3, v3 row_shr:4 row_mask:0xf bank_mask:0xf bound_ctrl:1
	s_nop 1
	v_add_f32_dpp v3, v3, v3 row_shr:8 row_mask:0xf bank_mask:0xf bound_ctrl:1
	s_nop 1
	v_mov_b32_dpp v13, v3 row_bcast:15 row_mask:0xa bank_mask:0xf
	v_add_f32_e32 v3, v3, v13
	v_mov_b32_e32 v13, 0
	s_nop 1
	v_mov_b32_dpp v13, v3 row_bcast:31 row_mask:0xc bank_mask:0xf
	v_add_f32_e32 v3, v3, v13
	s_nop 0
	v_readlane_b32 s47, v3, 63
	v_mov_b32_e32 v3, s35
	s_and_saveexec_b64 s[48:49], s[26:27]
	ds_add_rtn_u32 v3, v101, v116
	s_or_b64 exec, exec, s[48:49]
	s_waitcnt lgkmcnt(0)
	s_barrier
	s_and_saveexec_b64 s[48:49], s[0:1]
	s_cbranch_execz .LBB0_2098
	ds_read_b32 v13, v100
	s_waitcnt lgkmcnt(0)
	global_atomic_add v13, v[64:65], v13, off offset:256 sc0
	s_waitcnt vmcnt(0)
	ds_write_b32 v102, v13
